# deleted the dead zero-init v_mov in front of every fp8 pack pair (low-half + op_sel high-half converts define all 32 bits): 87 sites in hooks, moe-up epilogue, router norm
# baseline (speedup 1.0000x reference)
; #define GAS __attribute__((address_space(1)))
; #define LAS __attribute__((address_space(3)))
; #define LDS_BARRIER() do { asm volatile("s_waitcnt lgkmcnt(0)" ::: "memory"); __builtin_amdgcn_s_barrier(); asm volatile("" ::: "memory"); } while (0)
; template <class RowMap>
; __device__ __forceinline__ void conv_store_fp8(const f32x4 (&r)[8], unsigned char* WT, int Kbytes, int k0bytes, int n0, const RowMap rm, LAS unsigned char* T, int tid, int wave, int lane) {
;     ...
;     for (int j = 0; j < 4; ++j) { const unsigned lo = pk4_fp8(r[0][j] * W8_SCALE, r[1][j] * W8_SCALE, r[2][j] * W8_SCALE, r[3][j] * W8_SCALE), hi = pk4_fp8(r[4][j] * W8_SCALE, r[5][j] * W8_SCALE, r[6][j] * W8_SCALE, r[7][j] * W8_SCALE);
;         *(LAS unsigned long long*)(T + (4 * lane + j) * 64 + 8 * (wave ^ s)) = (unsigned long long)lo | ((unsigned long long)hi << 32); }
;     LDS_BARRIER();
;     const int c16 = tid & 3, rr = tid >> 2;
; #pragma unroll
;     for (int q = 0; q < 2; ++q) { const int row = rr + 128 * q; const v4u v = *(const LAS v4u*)(T + row * 64 + 16 * (c16 ^ ((row >> 2) & 3)));
;         const int dr = rm(n0 + row); if (dr >= 0) *(GAS v4u*)(WT + (unsigned)((((dr >> 8) * (Kbytes >> 7) + (k0bytes >> 7)) << 15) + ((dr & 255) << 7) + (k0bytes & 127) + 16 * c16)) = v; }
.Lhw_done_2:
	v_med3_f32 v131, v2, s101, v200
	v_med3_f32 v149, v6, s101, v200
	v_cvt_scalef32_pk_fp8_f32 v132, v131, v149, v201
	v_med3_f32 v133, v10, s101, v200
	v_med3_f32 v148, v14, s101, v200
	v_cvt_scalef32_pk_fp8_f32 v132, v133, v148, v201 op_sel:[0,0,0,1]
	v_med3_f32 v131, v18, s101, v200
	v_med3_f32 v165, v22, s101, v200
	v_cvt_scalef32_pk_fp8_f32 v133, v131, v165, v201
	v_med3_f32 v148, v30, s101, v200
	v_med3_f32 v149, v26, s101, v200
	v_cvt_scalef32_pk_fp8_f32 v133, v148, v149, v201 op_sel:[0,0,0,1]
	v_med3_f32 v131, v3, s101, v200
	v_med3_f32 v166, v7, s101, v200
	v_cvt_scalef32_pk_fp8_f32 v148, v131, v166, v201
	v_med3_f32 v149, v11, s101, v200
	v_med3_f32 v165, v15, s101, v200
	v_cvt_scalef32_pk_fp8_f32 v148, v149, v165, v201 op_sel:[0,0,0,1]
	v_med3_f32 v131, v19, s101, v200
	v_med3_f32 v167, v23, s101, v200
	v_cvt_scalef32_pk_fp8_f32 v149, v131, v167, v201
	v_med3_f32 v165, v31, s101, v200
	v_med3_f32 v166, v27, s101, v200
	v_cvt_scalef32_pk_fp8_f32 v149, v165, v166, v201 op_sel:[0,0,0,1]
	v_med3_f32 v131, v4, s101, v200
	s_cmp_lg_u32 s1, 0
	ds_write2_b64 v164, v[132:133], v[148:149] offset1:8
	v_med3_f32 v149, v8, s101, v200
	v_cvt_scalef32_pk_fp8_f32 v132, v131, v149, v201
	v_med3_f32 v133, v12, s101, v200
	v_med3_f32 v148, v16, s101, v200
	v_cvt_scalef32_pk_fp8_f32 v132, v133, v148, v201 op_sel:[0,0,0,1]
	v_med3_f32 v131, v20, s101, v200
	v_med3_f32 v165, v24, s101, v200
	v_cvt_scalef32_pk_fp8_f32 v133, v131, v165, v201
	v_med3_f32 v148, v32, s101, v200
	v_med3_f32 v149, v28, s101, v200
	v_cvt_scalef32_pk_fp8_f32 v133, v148, v149, v201 op_sel:[0,0,0,1]
	v_med3_f32 v131, v5, s101, v200
	v_med3_f32 v166, v9, s101, v200
	v_cvt_scalef32_pk_fp8_f32 v148, v131, v166, v201
	v_med3_f32 v149, v13, s101, v200
	v_med3_f32 v165, v17, s101, v200
	v_cvt_scalef32_pk_fp8_f32 v148, v149, v165, v201 op_sel:[0,0,0,1]
	v_med3_f32 v131, v21, s101, v200
	v_med3_f32 v167, v25, s101, v200
	v_cvt_scalef32_pk_fp8_f32 v149, v131, v167, v201
	v_med3_f32 v165, v33, s101, v200
	v_med3_f32 v166, v29, s101, v200
	v_cvt_scalef32_pk_fp8_f32 v149, v165, v166, v201 op_sel:[0,0,0,1]
	v_add_u32_e32 v131, s0, v156
	ds_write2_b64 v164, v[132:133], v[148:149] offset0:16 offset1:24
	s_cbranch_scc0 .LBB0_834
	s_lshl_b32 s6, s1, 7
	v_lshlrev_b32_e32 v148, 1, v131
	s_waitcnt lgkmcnt(0)
	s_barrier
	s_add_i32 s24, s6, 0xffffff00
	v_and_b32_e32 v133, 0x7f, v131
	v_and_b32_e32 v148, 0xffffff00, v148
	s_and_b32 s7, s64, 0x7f
	v_add_u32_e32 v148, s24, v148
	v_or_b32_e32 v133, s6, v133
	s_lshr_b32 s13, s64, 7
	v_add_u32_e32 v132, s7, v158
	v_cmp_lt_i32_e32 vcc, -1, v148
	v_lshlrev_b32_e32 v133, 7, v133
	v_add_u32_e32 v174, v157, v161
	ds_read_b128 v[170:173], v174
	s_and_saveexec_b64 s[6:7], vcc
	s_cbranch_execz .LBB0_831
	v_add_u32_e32 v149, v157, v159
	ds_read_b128 v[166:169], v149
	v_lshrrev_b32_e32 v148, 8, v148
	v_mul_u32_u24_e32 v148, s12, v148
	v_add_lshl_u32 v148, v148, s13, 15
	v_and_b32_e32 v149, 0x7f80, v133
	v_add3_u32 v148, v149, v132, v148
	s_waitcnt lgkmcnt(0)
	global_store_dwordx4 v148, v[166:169], s[40:41]

; #define GAS __attribute__((address_space(1)))
; #define LAS __attribute__((address_space(3)))
; #define LDS_BARRIER() do { asm volatile("s_waitcnt lgkmcnt(0)" ::: "memory"); __builtin_amdgcn_s_barrier(); asm volatile("" ::: "memory"); } while (0)
; template <class RowMap>
; __device__ __forceinline__ void conv_store_fp8(const f32x4 (&r)[8], unsigned char* WT, int Kbytes, int k0bytes, int n0, const RowMap rm, LAS unsigned char* T, int tid, int wave, int lane) {
;     ...
;     for (int j = 0; j < 4; ++j) { const unsigned lo = pk4_fp8(r[0][j] * W8_SCALE, r[1][j] * W8_SCALE, r[2][j] * W8_SCALE, r[3][j] * W8_SCALE), hi = pk4_fp8(r[4][j] * W8_SCALE, r[5][j] * W8_SCALE, r[6][j] * W8_SCALE, r[7][j] * W8_SCALE);
;         *(LAS unsigned long long*)(T + (4 * lane + j) * 64 + 8 * (wave ^ s)) = (unsigned long long)lo | ((unsigned long long)hi << 32); }
;     LDS_BARRIER();
;     const int c16 = tid & 3, rr = tid >> 2;
; #pragma unroll
;     for (int q = 0; q < 2; ++q) { const int row = rr + 128 * q; const v4u v = *(const LAS v4u*)(T + row * 64 + 16 * (c16 ^ ((row >> 2) & 3)));
;         const int dr = rm(n0 + row); if (dr >= 0) *(GAS v4u*)(WT + (unsigned)((((dr >> 8) * (Kbytes >> 7) + (k0bytes >> 7)) << 15) + ((dr & 255) << 7) + (k0bytes & 127) + 16 * c16)) = v; }
.Lhw_done_3:
	v_med3_f32 v131, v38, s101, v200
	v_med3_f32 v149, v42, s101, v200
	v_cvt_scalef32_pk_fp8_f32 v132, v131, v149, v201
	v_med3_f32 v133, v34, s101, v200
	v_med3_f32 v148, v46, s101, v200
	v_cvt_scalef32_pk_fp8_f32 v132, v133, v148, v201 op_sel:[0,0,0,1]
	v_med3_f32 v131, v50, s101, v200
	v_med3_f32 v165, v54, s101, v200
	v_cvt_scalef32_pk_fp8_f32 v133, v131, v165, v201
	v_med3_f32 v148, v62, s101, v200
	v_med3_f32 v149, v58, s101, v200
	v_cvt_scalef32_pk_fp8_f32 v133, v148, v149, v201 op_sel:[0,0,0,1]
	v_med3_f32 v131, v39, s101, v200
	v_med3_f32 v166, v43, s101, v200
	v_cvt_scalef32_pk_fp8_f32 v148, v131, v166, v201
	v_med3_f32 v149, v35, s101, v200
	v_med3_f32 v165, v47, s101, v200
	v_cvt_scalef32_pk_fp8_f32 v148, v149, v165, v201 op_sel:[0,0,0,1]
	v_med3_f32 v131, v51, s101, v200
	v_med3_f32 v167, v55, s101, v200
	v_cvt_scalef32_pk_fp8_f32 v149, v131, v167, v201
	v_med3_f32 v165, v63, s101, v200
	v_med3_f32 v166, v59, s101, v200
	v_cvt_scalef32_pk_fp8_f32 v149, v165, v166, v201 op_sel:[0,0,0,1]
	v_med3_f32 v131, v40, s101, v200
	s_cmp_lg_u32 s57, 0
	ds_write2_b64 v164, v[132:133], v[148:149] offset1:8
	v_med3_f32 v149, v44, s101, v200
	v_cvt_scalef32_pk_fp8_f32 v132, v131, v149, v201
	v_med3_f32 v133, v36, s101, v200
	v_med3_f32 v148, v48, s101, v200
	v_cvt_scalef32_pk_fp8_f32 v132, v133, v148, v201 op_sel:[0,0,0,1]
	v_med3_f32 v131, v52, s101, v200
	v_med3_f32 v165, v56, s101, v200
	v_cvt_scalef32_pk_fp8_f32 v133, v131, v165, v201
	v_med3_f32 v148, v64, s101, v200
	v_med3_f32 v149, v60, s101, v200
	v_cvt_scalef32_pk_fp8_f32 v133, v148, v149, v201 op_sel:[0,0,0,1]
	v_med3_f32 v131, v41, s101, v200
	v_med3_f32 v166, v45, s101, v200
	v_cvt_scalef32_pk_fp8_f32 v148, v131, v166, v201
	v_med3_f32 v149, v37, s101, v200
	v_med3_f32 v165, v49, s101, v200
	v_cvt_scalef32_pk_fp8_f32 v148, v149, v165, v201 op_sel:[0,0,0,1]
	v_med3_f32 v131, v53, s101, v200
	v_med3_f32 v167, v57, s101, v200
	v_cvt_scalef32_pk_fp8_f32 v149, v131, v167, v201
	v_med3_f32 v165, v65, s101, v200
	v_med3_f32 v166, v61, s101, v200
	v_cvt_scalef32_pk_fp8_f32 v149, v165, v166, v201 op_sel:[0,0,0,1]
	v_add_u32_e32 v131, s56, v156
	ds_write2_b64 v164, v[132:133], v[148:149] offset0:16 offset1:24
	s_cbranch_scc0 .LBB0_870
	s_lshl_b32 s6, s57, 7
	v_lshlrev_b32_e32 v148, 1, v131
	s_waitcnt lgkmcnt(0)
	s_barrier
	s_add_i32 s24, s6, 0xffffff00
	v_and_b32_e32 v133, 0x7f, v131
	v_and_b32_e32 v148, 0xffffff00, v148
	s_and_b32 s7, s58, 0x7f
	v_add_u32_e32 v148, s24, v148
	v_or_b32_e32 v133, s6, v133
	s_lshr_b32 s13, s58, 7
	v_add_u32_e32 v132, s7, v158
	v_cmp_lt_i32_e32 vcc, -1, v148
	v_lshlrev_b32_e32 v133, 7, v133
	v_add_u32_e32 v174, v157, v161
	ds_read_b128 v[170:173], v174
	s_and_saveexec_b64 s[6:7], vcc
	s_cbranch_execz .LBB0_867
	v_add_u32_e32 v149, v157, v159
	ds_read_b128 v[166:169], v149
	v_lshrrev_b32_e32 v148, 8, v148
	v_mul_u32_u24_e32 v148, s12, v148
	v_add_lshl_u32 v148, v148, s13, 15
	v_and_b32_e32 v149, 0x7f80, v133
	v_add3_u32 v148, v149, v132, v148
	s_waitcnt lgkmcnt(0)
	global_store_dwordx4 v148, v[166:169], s[86:87]

; #define GAS __attribute__((address_space(1)))
; #define LAS __attribute__((address_space(3)))
; #define LDS_BARRIER() do { asm volatile("s_waitcnt lgkmcnt(0)" ::: "memory"); __builtin_amdgcn_s_barrier(); asm volatile("" ::: "memory"); } while (0)
; template <class RowMap>
; __device__ __forceinline__ void conv_store_fp8(const f32x4 (&r)[8], unsigned char* WT, int Kbytes, int k0bytes, int n0, const RowMap rm, LAS unsigned char* T, int tid, int wave, int lane) {
;     ...
;     for (int j = 0; j < 4; ++j) { const unsigned lo = pk4_fp8(r[0][j] * W8_SCALE, r[1][j] * W8_SCALE, r[2][j] * W8_SCALE, r[3][j] * W8_SCALE), hi = pk4_fp8(r[4][j] * W8_SCALE, r[5][j] * W8_SCALE, r[6][j] * W8_SCALE, r[7][j] * W8_SCALE);
;         *(LAS unsigned long long*)(T + (4 * lane + j) * 64 + 8 * (wave ^ s)) = (unsigned long long)lo | ((unsigned long long)hi << 32); }
;     LDS_BARRIER();
;     const int c16 = tid & 3, rr = tid >> 2;
; #pragma unroll
;     for (int q = 0; q < 2; ++q) { const int row = rr + 128 * q; const v4u v = *(const LAS v4u*)(T + row * 64 + 16 * (c16 ^ ((row >> 2) & 3)));
;         const int dr = rm(n0 + row); if (dr >= 0) *(GAS v4u*)(WT + (unsigned)((((dr >> 8) * (Kbytes >> 7) + (k0bytes >> 7)) << 15) + ((dr & 255) << 7) + (k0bytes & 127) + 16 * c16)) = v; }
.Lhw_done_4:
	v_med3_f32 v131, v70, s101, v200
	v_med3_f32 v149, v74, s101, v200
	v_cvt_scalef32_pk_fp8_f32 v132, v131, v149, v201
	v_med3_f32 v133, v66, s101, v200
	v_med3_f32 v148, v78, s101, v200
	v_cvt_scalef32_pk_fp8_f32 v132, v133, v148, v201 op_sel:[0,0,0,1]
	v_med3_f32 v131, v82, s101, v200
	v_med3_f32 v165, v86, s101, v200
	v_cvt_scalef32_pk_fp8_f32 v133, v131, v165, v201
	v_med3_f32 v148, v94, s101, v200
	v_med3_f32 v149, v90, s101, v200
	v_cvt_scalef32_pk_fp8_f32 v133, v148, v149, v201 op_sel:[0,0,0,1]
	v_med3_f32 v131, v71, s101, v200
	v_med3_f32 v166, v75, s101, v200
	v_cvt_scalef32_pk_fp8_f32 v148, v131, v166, v201
	v_med3_f32 v149, v67, s101, v200
	v_med3_f32 v165, v79, s101, v200
	v_cvt_scalef32_pk_fp8_f32 v148, v149, v165, v201 op_sel:[0,0,0,1]
	v_med3_f32 v131, v83, s101, v200
	v_med3_f32 v167, v87, s101, v200
	v_cvt_scalef32_pk_fp8_f32 v149, v131, v167, v201
	v_med3_f32 v165, v95, s101, v200
	v_med3_f32 v166, v91, s101, v200
	v_cvt_scalef32_pk_fp8_f32 v149, v165, v166, v201 op_sel:[0,0,0,1]
	v_med3_f32 v131, v72, s101, v200
	s_cmp_lg_u32 s27, 0
	ds_write2_b64 v164, v[132:133], v[148:149] offset1:8
	v_med3_f32 v149, v76, s101, v200
	v_cvt_scalef32_pk_fp8_f32 v132, v131, v149, v201
	v_med3_f32 v133, v68, s101, v200
	v_med3_f32 v148, v80, s101, v200
	v_cvt_scalef32_pk_fp8_f32 v132, v133, v148, v201 op_sel:[0,0,0,1]
	v_med3_f32 v131, v84, s101, v200
	v_med3_f32 v165, v88, s101, v200
	v_cvt_scalef32_pk_fp8_f32 v133, v131, v165, v201
	v_med3_f32 v148, v96, s101, v200
	v_med3_f32 v149, v92, s101, v200
	v_cvt_scalef32_pk_fp8_f32 v133, v148, v149, v201 op_sel:[0,0,0,1]
	v_med3_f32 v131, v73, s101, v200
	v_med3_f32 v166, v77, s101, v200
	v_cvt_scalef32_pk_fp8_f32 v148, v131, v166, v201
	v_med3_f32 v149, v69, s101, v200
	v_med3_f32 v165, v81, s101, v200
	v_cvt_scalef32_pk_fp8_f32 v148, v149, v165, v201 op_sel:[0,0,0,1]
	v_med3_f32 v131, v85, s101, v200
	v_med3_f32 v167, v89, s101, v200
	v_cvt_scalef32_pk_fp8_f32 v149, v131, v167, v201
	v_med3_f32 v165, v97, s101, v200
	v_med3_f32 v166, v93, s101, v200
	v_cvt_scalef32_pk_fp8_f32 v149, v165, v166, v201 op_sel:[0,0,0,1]
	v_add_u32_e32 v131, s20, v156
	ds_write2_b64 v164, v[132:133], v[148:149] offset0:16 offset1:24
	s_cbranch_scc0 .LBB0_905
	s_lshl_b32 s6, s27, 7
	v_lshlrev_b32_e32 v148, 1, v131
	s_waitcnt lgkmcnt(0)
	s_barrier
	s_add_i32 s24, s6, 0xffffff00
	v_and_b32_e32 v133, 0x7f, v131
	v_and_b32_e32 v148, 0xffffff00, v148
	s_and_b32 s7, s29, 0x7f
	v_add_u32_e32 v148, s24, v148
	v_or_b32_e32 v133, s6, v133
	s_lshr_b32 s13, s29, 7
	v_add_u32_e32 v132, s7, v158
	v_cmp_lt_i32_e32 vcc, -1, v148
	v_lshlrev_b32_e32 v133, 7, v133
	v_add_u32_e32 v174, v157, v161
	ds_read_b128 v[170:173], v174
	s_and_saveexec_b64 s[6:7], vcc
	s_cbranch_execz .LBB0_902
	v_add_u32_e32 v149, v157, v159
	ds_read_b128 v[166:169], v149
	v_lshrrev_b32_e32 v148, 8, v148
	v_mul_u32_u24_e32 v148, s12, v148
	v_add_lshl_u32 v148, v148, s13, 15
	v_and_b32_e32 v149, 0x7f80, v133
	v_add3_u32 v148, v149, v132, v148
	s_waitcnt lgkmcnt(0)
	global_store_dwordx4 v148, v[166:169], s[90:91]

; #define GAS __attribute__((address_space(1)))
; #define LAS __attribute__((address_space(3)))
; #define LDS_BARRIER() do { asm volatile("s_waitcnt lgkmcnt(0)" ::: "memory"); __builtin_amdgcn_s_barrier(); asm volatile("" ::: "memory"); } while (0)
; template <class RowMap>
; __device__ __forceinline__ void conv_store_fp8(const f32x4 (&r)[8], unsigned char* WT, int Kbytes, int k0bytes, int n0, const RowMap rm, LAS unsigned char* T, int tid, int wave, int lane) {
;     ...
;     for (int j = 0; j < 4; ++j) { const unsigned lo = pk4_fp8(r[0][j] * W8_SCALE, r[1][j] * W8_SCALE, r[2][j] * W8_SCALE, r[3][j] * W8_SCALE), hi = pk4_fp8(r[4][j] * W8_SCALE, r[5][j] * W8_SCALE, r[6][j] * W8_SCALE, r[7][j] * W8_SCALE);
;         *(LAS unsigned long long*)(T + (4 * lane + j) * 64 + 8 * (wave ^ s)) = (unsigned long long)lo | ((unsigned long long)hi << 32); }
;     LDS_BARRIER();
;     const int c16 = tid & 3, rr = tid >> 2;
; #pragma unroll
;     for (int q = 0; q < 2; ++q) { const int row = rr + 128 * q; const v4u v = *(const LAS v4u*)(T + row * 64 + 16 * (c16 ^ ((row >> 2) & 3)));
;         const int dr = rm(n0 + row); if (dr >= 0) *(GAS v4u*)(WT + (unsigned)((((dr >> 8) * (Kbytes >> 7) + (k0bytes >> 7)) << 15) + ((dr & 255) << 7) + (k0bytes & 127) + 16 * c16)) = v; }
.Lhw_done_5:
	v_med3_f32 v131, v102, s101, v200
	v_med3_f32 v149, v106, s101, v200
	v_cvt_scalef32_pk_fp8_f32 v132, v131, v149, v201
	v_med3_f32 v133, v98, s101, v200
	v_med3_f32 v148, v110, s101, v200
	v_cvt_scalef32_pk_fp8_f32 v132, v133, v148, v201 op_sel:[0,0,0,1]
	v_med3_f32 v131, v114, s101, v200
	v_med3_f32 v165, v118, s101, v200
	v_cvt_scalef32_pk_fp8_f32 v133, v131, v165, v201
	v_med3_f32 v148, v126, s101, v200
	v_med3_f32 v149, v122, s101, v200
	v_cvt_scalef32_pk_fp8_f32 v133, v148, v149, v201 op_sel:[0,0,0,1]
	v_med3_f32 v131, v103, s101, v200
	v_med3_f32 v166, v107, s101, v200
	v_cvt_scalef32_pk_fp8_f32 v148, v131, v166, v201
	v_med3_f32 v149, v99, s101, v200
	v_med3_f32 v165, v111, s101, v200
	v_cvt_scalef32_pk_fp8_f32 v148, v149, v165, v201 op_sel:[0,0,0,1]
	v_med3_f32 v131, v115, s101, v200
	v_med3_f32 v167, v119, s101, v200
	v_cvt_scalef32_pk_fp8_f32 v149, v131, v167, v201
	v_med3_f32 v165, v127, s101, v200
	v_med3_f32 v166, v123, s101, v200
	v_cvt_scalef32_pk_fp8_f32 v149, v165, v166, v201 op_sel:[0,0,0,1]
	v_med3_f32 v131, v104, s101, v200
	s_cmp_lg_u32 s24, 0
	ds_write2_b64 v164, v[132:133], v[148:149] offset1:8
	v_med3_f32 v149, v108, s101, v200
	v_cvt_scalef32_pk_fp8_f32 v132, v131, v149, v201
	v_med3_f32 v133, v100, s101, v200
	v_med3_f32 v148, v112, s101, v200
	v_cvt_scalef32_pk_fp8_f32 v132, v133, v148, v201 op_sel:[0,0,0,1]
	v_med3_f32 v131, v116, s101, v200
	v_med3_f32 v165, v120, s101, v200
	v_cvt_scalef32_pk_fp8_f32 v133, v131, v165, v201
	v_med3_f32 v148, v128, s101, v200
	v_med3_f32 v149, v124, s101, v200
	v_cvt_scalef32_pk_fp8_f32 v133, v148, v149, v201 op_sel:[0,0,0,1]
	v_med3_f32 v131, v105, s101, v200
	v_med3_f32 v166, v109, s101, v200
	v_cvt_scalef32_pk_fp8_f32 v148, v131, v166, v201
	v_med3_f32 v149, v101, s101, v200
	v_med3_f32 v165, v113, s101, v200
	v_cvt_scalef32_pk_fp8_f32 v148, v149, v165, v201 op_sel:[0,0,0,1]
	v_med3_f32 v131, v117, s101, v200
	v_med3_f32 v167, v121, s101, v200
	v_cvt_scalef32_pk_fp8_f32 v149, v131, v167, v201
	v_med3_f32 v165, v129, s101, v200
	v_med3_f32 v166, v125, s101, v200
	v_cvt_scalef32_pk_fp8_f32 v149, v165, v166, v201 op_sel:[0,0,0,1]
	v_add_u32_e32 v131, s19, v156
	ds_write2_b64 v164, v[132:133], v[148:149] offset0:16 offset1:24
	s_cbranch_scc0 .LBB0_941
	s_waitcnt lgkmcnt(0)
	s_lshl_b32 s4, s24, 7
	v_lshlrev_b32_e32 v148, 1, v131
	s_waitcnt lgkmcnt(0)
	s_barrier
	s_add_i32 s7, s4, 0xffffff00
	v_and_b32_e32 v133, 0x7f, v131
	v_and_b32_e32 v148, 0xffffff00, v148
	s_and_b32 s5, s18, 0x7f
	v_add_u32_e32 v148, s7, v148
	v_or_b32_e32 v133, s4, v133
	s_lshr_b32 s6, s18, 7
	v_add_u32_e32 v132, s5, v158
	v_cmp_lt_i32_e32 vcc, -1, v148
	v_lshlrev_b32_e32 v133, 7, v133
	v_add_u32_e32 v174, v157, v161
	ds_read_b128 v[170:173], v174
	s_and_saveexec_b64 s[4:5], vcc
	s_cbranch_execz .LBB0_938
	v_add_u32_e32 v149, v157, v159
	ds_read_b128 v[166:169], v149
	v_lshrrev_b32_e32 v148, 8, v148
	v_mul_u32_u24_e32 v148, s2, v148
	v_add_lshl_u32 v148, v148, s6, 15
	v_and_b32_e32 v149, 0x7f80, v133
	v_add3_u32 v148, v149, v132, v148
	s_waitcnt lgkmcnt(0)
	global_store_dwordx4 v148, v[166:169], s[50:51]

; #define GAS __attribute__((address_space(1)))
; #define LAS __attribute__((address_space(3)))
; template <bool ROUTER, bool SMALLP>
; __device__ __forceinline__ void norm_phase(KA A, LAS unsigned char* lds, int l, int which, int npart, const float* pgate, int tid, int wave, int lane, int bid) {
;     ...
;         if (nb) {
; #pragma unroll
;             for (int jj = 0; jj < 4; ++jj) { float f[8]; unpack8(vnb[jj], f); v[2 * jj] = (f32x4){f[0], f[1], f[2], f[3]}; v[2 * jj + 1] = (f32x4){f[4], f[5], f[6], f[7]}; }
;         } else {
; #pragma unroll
;             for (int j = 0; j < 8; ++j) v[j] = vnx[j];
;         }
;         if (rl + NWAVES < 34) NORM_LOAD(rl + NWAVES);
;         if (isctx && npart > 0) {
;             f32x4 acc[8];
; #pragma unroll
;             for (int j = 0; j < 8; ++j) acc[j] = (f32x4){0.f, 0.f, 0.f, 0.f};
;             for (int p0 = 0; p0 < npart; p0 += 6) { v4u t[6][4];
; #pragma unroll
;                 for (int q = 0; q < 6; ++q) { const int p = (p0 + q < npart) ? p0 + q : p0; const GAS v4u* pr = (const GAS v4u*)(PART + ((size_t)p * 512 + b * CTXL + s) * D) + lane;
; #pragma unroll
;                     for (int jj = 0; jj < 4; ++jj) t[q][jj] = pr[64 * jj]; }
;                 SCHED_FENCE();
; #pragma unroll
;                 for (int q = 0; q < 6; ++q) if (p0 + q < npart) {
; #pragma unroll
;                     for (int jj = 0; jj < 4; ++jj) { float f[8]; unpack8(t[q][jj], f); acc[2 * jj] += (f32x4){f[0], f[1], f[2], f[3]}; acc[2 * jj + 1] += (f32x4){f[4], f[5], f[6], f[7]}; } } }
;             const GAS f32x4* gp = (const GAS f32x4*)pgate + 2 * lane; GAS v4u* hw = (GAS v4u*)(H + (size_t)row * D) + lane;
; #pragma unroll
;             for (int j = 0; j < 8; ++j) v[j] += gp[VIDX(j)] * acc[j];
; #pragma unroll
;             for (int jj = 0; jj < 4; ++jj) { const float f[8] = {v[2 * jj].x, v[2 * jj].y, v[2 * jj].z, v[2 * jj].w, v[2 * jj + 1].x, v[2 * jj + 1].y, v[2 * jj + 1].z, v[2 * jj + 1].w}; hw[64 * jj] = pack8(f); }
;         }
; #pragma unroll
;         for (int j = 0; j < 8; ++j) ss += (v[j].x * v[j].x + v[j].y * v[j].y) + (v[j].z * v[j].z + v[j].w * v[j].w);
;         const float rstd = __builtin_amdgcn_rsqf(wave_sum(ss) * (1.f / D) + EPS);
;         const LAS f32x4* ca = (const LAS f32x4*)(cA + (isctx ? D : 0)) + 2 * lane; const LAS f32x4* cb = (const LAS f32x4*)(cB + (isctx ? D : 0)) + 2 * lane;
.LBB0_1704:
	v_lshlrev_b32_e32 v51, 16, v32
	v_and_b32_e32 v65, 0xffff0000, v32
	v_and_b32_e32 v64, 0xffff0000, v30
	v_lshlrev_b32_e32 v67, 16, v33
	v_and_b32_e32 v33, 0xffff0000, v33
	v_and_b32_e32 v32, 0xffff0000, v31
	v_lshlrev_b32_e32 v50, 16, v30
	v_lshlrev_b32_e32 v66, 16, v31
	v_pk_mul_f32 v[44:45], v[64:65], v[64:65]
	v_pk_mul_f32 v[46:47], v[32:33], v[32:33]
	v_pk_fma_f32 v[44:45], v[50:51], v[50:51], v[44:45]
	v_pk_fma_f32 v[46:47], v[66:67], v[66:67], v[46:47]
	v_and_b32_e32 v71, 0xffff0000, v27
	v_and_b32_e32 v70, 0xffff0000, v26
	v_pk_add_f32 v[44:45], v[44:45], v[46:47]
	v_lshlrev_b32_e32 v69, 16, v27
	v_lshlrev_b32_e32 v68, 16, v26
	v_lshlrev_b32_e32 v72, 16, v28
	v_and_b32_e32 v73, 0xffff0000, v28
	v_lshlrev_b32_e32 v28, 16, v29
	v_lshlrev_b32_e32 v26, 16, v22
	v_pk_add_f32 v[44:45], v[44:45], v[44:45] op_sel_hi:[0,1]
	v_pk_mul_f32 v[46:47], v[70:71], v[70:71]
	v_and_b32_e32 v29, 0xffff0000, v29
	v_pk_fma_f32 v[46:47], v[68:69], v[68:69], v[46:47]
	v_mul_f32_e32 v27, v72, v72
	v_mul_f32_e32 v49, v73, v73
	v_mul_f32_e32 v44, v28, v28
	v_mov_b32_e32 v48, v26
	v_and_b32_e32 v57, 0xffff0000, v22
	v_lshlrev_b32_e32 v30, 16, v23
	v_and_b32_e32 v31, 0xffff0000, v23
	v_pk_add_f32 v[46:47], v[46:47], v[46:47] op_sel_hi:[0,1]
	v_pk_fma_f32 v[52:53], v[28:29], v[28:29], v[44:45] op_sel_hi:[1,1,0]
	v_pk_add_f32 v[48:49], v[26:27], v[48:49]
	v_mul_f32_e32 v52, v57, v57
	v_mul_f32_e32 v44, v30, v30
	v_mul_f32_e32 v46, v31, v31
	v_mul_f32_e32 v54, v26, v26
	v_mov_b32_e32 v55, v49
	v_pk_add_f32 v[48:49], v[54:55], v[52:53]
	v_pk_add_f32 v[44:45], v[44:45], v[46:47]
	v_lshlrev_b32_e32 v23, 16, v25
	v_lshlrev_b32_e32 v22, 16, v24
	v_and_b32_e32 v25, 0xffff0000, v25
	v_and_b32_e32 v24, 0xffff0000, v24
	v_pk_add_f32 v[44:45], v[48:49], v[44:45]
	v_lshlrev_b32_e32 v40, 16, v18
	v_and_b32_e32 v41, 0xffff0000, v18
	v_lshlrev_b32_e32 v42, 16, v19
	v_lshlrev_b32_e32 v18, 16, v20
	v_pk_add_f32 v[44:45], v[44:45], v[44:45] op_sel_hi:[0,1]
	v_pk_mul_f32 v[46:47], v[24:25], v[24:25]
	v_and_b32_e32 v43, 0xffff0000, v19
	v_pk_fma_f32 v[46:47], v[22:23], v[22:23], v[46:47]
	v_mul_f32_e32 v19, v40, v40
	v_mul_f32_e32 v49, v41, v41
	v_mul_f32_e32 v44, v42, v42
	v_mov_b32_e32 v48, v18
	v_and_b32_e32 v59, 0xffff0000, v20
	v_lshlrev_b32_e32 v20, 16, v21
	v_and_b32_e32 v21, 0xffff0000, v21
	v_pk_add_f32 v[46:47], v[46:47], v[46:47] op_sel_hi:[0,1]
	v_pk_fma_f32 v[52:53], v[42:43], v[42:43], v[44:45] op_sel_hi:[1,1,0]
	v_pk_add_f32 v[48:49], v[18:19], v[48:49]
	v_mul_f32_e32 v52, v59, v59
	v_mul_f32_e32 v46, v20, v20
	v_mul_f32_e32 v44, v21, v21
	v_mul_f32_e32 v54, v18, v18
	v_mov_b32_e32 v55, v49
	v_pk_add_f32 v[48:49], v[54:55], v[52:53]
	v_pk_add_f32 v[44:45], v[46:47], v[44:45]
	s_mul_hi_i32 s2, s4, 0x78787879
	v_pk_add_f32 v[44:45], v[48:49], v[44:45]
	s_lshr_b32 s5, s2, 31
	v_add_f32_e32 v19, v44, v45
	s_ashr_i32 s2, s2, 11
	s_add_i32 s2, s2, s5
	v_add_f32_dpp v19, v19, v19 quad_perm:[1,0,3,2] row_mask:0xf bank_mask:0xf bound_ctrl:1
	v_mov_b32_e32 v27, v130
	s_mulk_i32 s2, 0x1100
	v_add_f32_dpp v19, v19, v19 quad_perm:[2,3,0,1] row_mask:0xf bank_mask:0xf bound_ctrl:1
	s_sub_i32 s2, s4, s2
	s_cmpk_lt_i32 s2, 0x100
	v_add_f32_dpp v19, v19, v19 row_half_mirror row_mask:0xf bank_mask:0xf bound_ctrl:1
	s_cselect_b64 s[10:11], -1, 0
	s_and_b64 s[6:7], s[10:11], exec
	v_add_f32_dpp v19, v19, v19 row_mirror row_mask:0xf bank_mask:0xf bound_ctrl:1
	v_mov_b32_e32 v44, v50
	v_mov_b32_e32 v45, v64
	v_mov_b32_dpp v27, v19 row_bcast:15 row_mask:0xa bank_mask:0xf
	v_add_f32_e32 v19, v19, v27
	v_mov_b32_e32 v27, v130
	v_mov_b32_e32 v64, v51
	s_nop 0
	v_mov_b32_dpp v27, v19 row_bcast:31 row_mask:0xc bank_mask:0xf
	v_add_f32_e32 v19, v19, v27
	v_mov_b32_e32 v27, v57
	v_readlane_b32 s2, v19, 63
	v_mov_b32_e32 v19, 0x3a000000
	s_nop 0
	v_fma_f32 v19, s2, v19, v1
	s_cselect_b32 s2, 0x2000, 0
	v_rsq_f32_e32 v56, v19
	v_add_u32_e32 v76, s2, v35
	ds_read_b128 v[46:49], v76
	ds_read_b128 v[52:55], v76 offset:16
	ds_read_b128 v[60:63], v76 offset:16384
	v_mov_b32_e32 v19, v59
	v_pk_mul_f32 v[74:75], v[56:57], v[44:45] op_sel_hi:[0,1]
	v_mov_b32_e32 v44, v66
	v_mov_b32_e32 v45, v32
	v_pk_mul_f32 v[44:45], v[56:57], v[44:45] op_sel_hi:[0,1]
	s_waitcnt lgkmcnt(0)
	v_pk_fma_f32 v[44:45], v[48:49], v[44:45], v[62:63]
	ds_read_b128 v[48:51], v76 offset:16400
	v_mov_b32_e32 v32, v67
	v_pk_fma_f32 v[46:47], v[46:47], v[74:75], v[60:61]
	v_pk_mul_f32 v[60:61], v[56:57], v[64:65] op_sel_hi:[0,1]
	v_pk_mul_f32 v[32:33], v[56:57], v[32:33] op_sel_hi:[0,1]
	s_waitcnt lgkmcnt(0)
	v_pk_fma_f32 v[50:51], v[54:55], v[32:33], v[50:51]
	v_pk_fma_f32 v[54:55], v[52:53], v[60:61], v[48:49]
	ds_read_b128 v[60:63], v76 offset:2048
	ds_read_b128 v[64:67], v76 offset:18432
	v_mov_b32_e32 v32, v68
	v_mov_b32_e32 v33, v70
	v_mov_b32_e32 v70, v69
	v_pk_mul_f32 v[32:33], v[56:57], v[32:33] op_sel_hi:[0,1]
	v_pk_mul_f32 v[48:49], v[56:57], v[70:71] op_sel_hi:[0,1]
	s_waitcnt lgkmcnt(0)
	v_pk_fma_f32 v[48:49], v[62:63], v[48:49], v[66:67]
	v_pk_fma_f32 v[52:53], v[60:61], v[32:33], v[64:65]
	ds_read_b128 v[60:63], v76 offset:2064
	ds_read_b128 v[64:67], v76 offset:18448
	v_pk_mul_f32 v[32:33], v[56:57], v[72:73] op_sel_hi:[0,1]
	v_pk_mul_f32 v[28:29], v[56:57], v[28:29] op_sel_hi:[0,1]
	v_pk_mul_f32 v[68:69], v[56:57], v[26:27] op_sel_hi:[0,1]
	v_pk_mul_f32 v[26:27], v[56:57], v[30:31] op_sel_hi:[0,1]
	s_waitcnt lgkmcnt(0)
	v_pk_fma_f32 v[28:29], v[28:29], v[62:63], v[66:67]
	v_pk_fma_f32 v[32:33], v[32:33], v[60:61], v[64:65]
	ds_read_b128 v[60:63], v76 offset:4096
	ds_read_b128 v[64:67], v76 offset:20480
	v_mul_f32_e32 v59, 0x41800000, v46
	v_med3_f32 v59, v59, s62, v236
	s_ashr_i32 s5, s4, 31
	s_lshl_b64 s[4:5], s[4:5], 11
	s_waitcnt lgkmcnt(0)
; __device__ __forceinline__ unsigned cvt_pk_bf16(float lo, float hi) { unsigned r; asm volatile("v_cvt_pk_bf16_f32 %0, %1, %2" : "=v"(r) : "v"(lo), "v"(hi)); return r; }
; #define LAS __attribute__((address_space(3)))
; template <bool ROUTER, bool SMALLP>
; __device__ __forceinline__ void norm_phase(KA A, LAS unsigned char* lds, int l, int which, int npart, const float* pgate, int tid, int wave, int lane, int bid) {
;     ...
;         for (int j = 0; j < 8; ++j) v[j] = v[j] * rstd * ca[VIDX(j)] + cb[VIDX(j)];
; #pragma unroll
;         for (int jj = 0; jj < 4; ++jj) { const f32x4 x0 = v[2 * jj], x1 = v[2 * jj + 1];
;             if (ROUTER) o8[64 * jj] = (unsigned long long)pk4_fp8(x0.x * XN8_SCALE, x0.y * XN8_SCALE, x0.z * XN8_SCALE, x0.w * XN8_SCALE) | ((unsigned long long)pk4_fp8(x1.x * XN8_SCALE, x1.y * XN8_SCALE, x1.z * XN8_SCALE, x1.w * XN8_SCALE) << 32);
;             else { v4u o; o.x = pg8::cvt_pk_bf16(x0.x, x0.y); o.y = pg8::cvt_pk_bf16(x0.z, x0.w); o.z = pg8::cvt_pk_bf16(x1.x, x1.y); o.w = pg8::cvt_pk_bf16(x1.z, x1.w); o16[64 * jj] = o; } }
;         if (ROUTER) {
;             float lg[8];
; #pragma unroll
;             for (int e = 0; e < 8; ++e) { const LAS f32x4* wv = (const LAS f32x4*)(wrT + e * D) + 2 * lane; float a = 0.f;
; #pragma unroll
;                 for (int j = 0; j < 8; ++j) { const f32x4 w = wv[VIDX(j)]; a += (v[j].x * w.x + v[j].y * w.y) + (v[j].z * w.z + v[j].w * w.w); }
;                 lg[e] = wave_sum(a); }
	v_pk_fma_f32 v[30:31], v[68:69], v[60:61], v[64:65]
	v_mov_b32_e32 v60, v22
	v_mov_b32_e32 v61, v24
	v_pk_fma_f32 v[26:27], v[26:27], v[62:63], v[66:67]
	v_pk_mul_f32 v[68:69], v[56:57], v[60:61] op_sel_hi:[0,1]
	ds_read_b128 v[60:63], v76 offset:4112
	ds_read_b128 v[64:67], v76 offset:20496
	v_mov_b32_e32 v24, v23
	v_pk_mul_f32 v[22:23], v[56:57], v[24:25] op_sel_hi:[0,1]
	s_waitcnt lgkmcnt(0)
	v_pk_fma_f32 v[22:23], v[22:23], v[62:63], v[66:67]
	v_pk_fma_f32 v[24:25], v[68:69], v[60:61], v[64:65]
	ds_read_b128 v[60:63], v76 offset:6144
	ds_read_b128 v[64:67], v76 offset:22528
	v_pk_mul_f32 v[68:69], v[56:57], v[40:41] op_sel_hi:[0,1]
	v_pk_mul_f32 v[40:41], v[56:57], v[42:43] op_sel_hi:[0,1]
	s_waitcnt lgkmcnt(0)
	v_pk_fma_f32 v[40:41], v[40:41], v[62:63], v[66:67]
	v_pk_fma_f32 v[42:43], v[68:69], v[60:61], v[64:65]
	ds_read_b128 v[60:63], v76 offset:6160
	ds_read_b128 v[64:67], v76 offset:22544
	v_pk_mul_f32 v[68:69], v[56:57], v[18:19] op_sel_hi:[0,1]
	v_pk_mul_f32 v[18:19], v[56:57], v[20:21] op_sel_hi:[0,1]
	v_lshl_add_u64 v[56:57], v[38:39], 0, s[4:5]
	s_waitcnt lgkmcnt(0)
	v_pk_fma_f32 v[20:21], v[68:69], v[60:61], v[64:65]
	v_mul_f32_e32 v60, 0x41800000, v47
	v_pk_fma_f32 v[18:19], v[18:19], v[62:63], v[66:67]
	v_med3_f32 v63, v60, s62, v236
	v_cvt_pk_fp8_f32 v60, v59, v63
	v_mul_f32_e32 v61, 0x41800000, v44
	v_mul_f32_e32 v62, 0x41800000, v45
	v_med3_f32 v61, v61, s62, v236
	v_med3_f32 v62, v62, s62, v236
	v_cvt_pk_fp8_f32 v60, v61, v62 op_sel:[0,0,1]
	v_mul_f32_e32 v59, 0x41800000, v54
	v_mul_f32_e32 v61, 0x41800000, v55
	v_med3_f32 v59, v59, s62, v236
	v_med3_f32 v64, v61, s62, v236
	v_cvt_pk_fp8_f32 v61, v59, v64
	v_mul_f32_e32 v62, 0x41800000, v50
	v_mul_f32_e32 v63, 0x41800000, v51
	v_med3_f32 v62, v62, s62, v236
	v_med3_f32 v63, v63, s62, v236
	v_cvt_pk_fp8_f32 v61, v62, v63 op_sel:[0,0,1]
	v_mul_f32_e32 v59, 0x41800000, v52
	v_med3_f32 v59, v59, s62, v236
	v_mul_f32_e32 v62, 0x41800000, v49
	global_store_dwordx2 v[56:57], v[60:61], off
	v_mul_f32_e32 v60, 0x41800000, v53
	v_med3_f32 v63, v60, s62, v236
	v_cvt_pk_fp8_f32 v60, v59, v63
	v_mul_f32_e32 v61, 0x41800000, v48
	v_med3_f32 v61, v61, s62, v236
	v_med3_f32 v62, v62, s62, v236
	v_cvt_pk_fp8_f32 v60, v61, v62 op_sel:[0,0,1]
	v_mul_f32_e32 v59, 0x41800000, v32
	v_mul_f32_e32 v61, 0x41800000, v33
	v_med3_f32 v59, v59, s62, v236
	v_med3_f32 v64, v61, s62, v236
	v_cvt_pk_fp8_f32 v61, v59, v64
	v_mul_f32_e32 v62, 0x41800000, v28
	v_mul_f32_e32 v63, 0x41800000, v29
	v_med3_f32 v62, v62, s62, v236
	v_med3_f32 v63, v63, s62, v236
	v_cvt_pk_fp8_f32 v61, v62, v63 op_sel:[0,0,1]
	v_mul_f32_e32 v59, 0x41800000, v30
	v_med3_f32 v59, v59, s62, v236
	v_mul_f32_e32 v62, 0x41800000, v27
	global_store_dwordx2 v[56:57], v[60:61], off offset:512
	v_mul_f32_e32 v60, 0x41800000, v31
	v_med3_f32 v63, v60, s62, v236
	v_cvt_pk_fp8_f32 v60, v59, v63
	v_mul_f32_e32 v61, 0x41800000, v26
	v_med3_f32 v61, v61, s62, v236
	v_med3_f32 v62, v62, s62, v236
	v_cvt_pk_fp8_f32 v60, v61, v62 op_sel:[0,0,1]
	v_mul_f32_e32 v59, 0x41800000, v24
	v_mul_f32_e32 v61, 0x41800000, v25
	v_med3_f32 v59, v59, s62, v236
	v_med3_f32 v64, v61, s62, v236
	v_cvt_pk_fp8_f32 v61, v59, v64
	v_mul_f32_e32 v62, 0x41800000, v22
	v_mul_f32_e32 v63, 0x41800000, v23
	v_med3_f32 v62, v62, s62, v236
	v_med3_f32 v63, v63, s62, v236
	v_cvt_pk_fp8_f32 v61, v62, v63 op_sel:[0,0,1]
	v_mul_f32_e32 v59, 0x41800000, v42
	v_med3_f32 v59, v59, s62, v236
	v_mul_f32_e32 v62, 0x41800000, v41
	global_store_dwordx2 v[56:57], v[60:61], off offset:1024
	v_mul_f32_e32 v60, 0x41800000, v43
	v_med3_f32 v63, v60, s62, v236
	v_cvt_pk_fp8_f32 v60, v59, v63
	v_mul_f32_e32 v61, 0x41800000, v40
	v_med3_f32 v61, v61, s62, v236
	v_med3_f32 v62, v62, s62, v236
	v_cvt_pk_fp8_f32 v60, v61, v62 op_sel:[0,0,1]
	v_mul_f32_e32 v59, 0x41800000, v20
	v_mul_f32_e32 v61, 0x41800000, v21
	v_med3_f32 v59, v59, s62, v236
	v_med3_f32 v64, v61, s62, v236
	v_cvt_pk_fp8_f32 v61, v59, v64
	v_mul_f32_e32 v62, 0x41800000, v18
	v_mul_f32_e32 v63, 0x41800000, v19
	v_med3_f32 v62, v62, s62, v236
	v_med3_f32 v63, v63, s62, v236
	v_cvt_pk_fp8_f32 v61, v62, v63 op_sel:[0,0,1]
	global_store_dwordx2 v[56:57], v[60:61], off offset:1536
	ds_read_b128 v[60:63], v35 offset:32768
	ds_read_b128 v[64:67], v35 offset:32784
	s_waitcnt lgkmcnt(1)
	v_mul_f32_e32 v56, v47, v61
	v_mul_f32_e32 v57, v45, v63
	v_fmac_f32_e32 v56, v46, v60
	v_fmac_f32_e32 v57, v44, v62
	ds_read_b128 v[60:63], v35 offset:34816
	v_add_f32_e32 v56, v56, v57
	s_waitcnt lgkmcnt(1)
	v_mul_f32_e32 v57, v55, v65
	v_mul_f32_e32 v59, v51, v67
	v_fmac_f32_e32 v57, v54, v64
	v_fmac_f32_e32 v59, v50, v66
	v_add_f32_e32 v56, 0, v56
	v_add_f32_e32 v57, v57, v59
	v_add_f32_e32 v56, v56, v57
	s_waitcnt lgkmcnt(0)
	v_mul_f32_e32 v57, v53, v61
	v_mul_f32_e32 v59, v49, v63
	v_fmac_f32_e32 v57, v52, v60
	v_fmac_f32_e32 v59, v48, v62
	ds_read_b128 v[60:63], v35 offset:34832
	v_add_f32_e32 v57, v57, v59
	v_add_f32_e32 v56, v56, v57
	s_waitcnt lgkmcnt(0)
	v_mul_f32_e32 v57, v33, v61
	v_mul_f32_e32 v59, v29, v63
	v_fmac_f32_e32 v57, v32, v60
	v_fmac_f32_e32 v59, v28, v62
	ds_read_b128 v[60:63], v35 offset:36864
	v_add_f32_e32 v57, v57, v59
	v_add_f32_e32 v56, v56, v57
	s_waitcnt lgkmcnt(0)
	v_mul_f32_e32 v57, v31, v61
	v_mul_f32_e32 v59, v27, v63
	v_fmac_f32_e32 v57, v30, v60
	v_fmac_f32_e32 v59, v26, v62
	ds_read_b128 v[60:63], v35 offset:36880
	v_add_f32_e32 v57, v57, v59
	v_add_f32_e32 v56, v56, v57
	s_waitcnt lgkmcnt(0)
	v_mul_f32_e32 v57, v25, v61
	v_mul_f32_e32 v59, v23, v63
	v_fmac_f32_e32 v57, v24, v60
	v_fmac_f32_e32 v59, v22, v62
	ds_read_b128 v[60:63], v35 offset:38912
	v_add_f32_e32 v57, v57, v59
	v_add_f32_e32 v56, v56, v57
	s_waitcnt lgkmcnt(0)
; #define LAS __attribute__((address_space(3)))
; template <int CTRL, int ROWMASK> __device__ __forceinline__ float dpp_f(float v) { return __int_as_float(__builtin_amdgcn_update_dpp(0, __float_as_int(v), CTRL, ROWMASK, 0xF, false)); }
; __device__ __forceinline__ float row16_sum(float v) { v += dpp_f<0xB1, 0xF>(v); v += dpp_f<0x4E, 0xF>(v); v += dpp_f<0x141, 0xF>(v); v += dpp_f<0x140, 0xF>(v); return v; }
; __device__ __forceinline__ float wave_sum(float v) {
;     v = row16_sum(v); v += dpp_f<0x142, 0xA>(v); v += dpp_f<0x143, 0xC>(v);
;     return __int_as_float(__builtin_amdgcn_readlane(__float_as_int(v), 63));
; }
; template <bool ROUTER, bool SMALLP>
; __device__ __forceinline__ void norm_phase(KA A, LAS unsigned char* lds, int l, int which, int npart, const float* pgate, int tid, int wave, int lane, int bid) {
;     ...
;             for (int e = 0; e < 8; ++e) { const LAS f32x4* wv = (const LAS f32x4*)(wrT + e * D) + 2 * lane; float a = 0.f;
; #pragma unroll
;                 for (int j = 0; j < 8; ++j) { const f32x4 w = wv[VIDX(j)]; a += (v[j].x * w.x + v[j].y * w.y) + (v[j].z * w.z + v[j].w * w.w); }
;                 lg[e] = wave_sum(a); }
	v_mul_f32_e32 v57, v43, v61
	v_mul_f32_e32 v59, v41, v63
	v_fmac_f32_e32 v57, v42, v60
	v_fmac_f32_e32 v59, v40, v62
	ds_read_b128 v[60:63], v35 offset:38928
	v_add_f32_e32 v57, v57, v59
	v_add_f32_e32 v56, v56, v57
	s_waitcnt lgkmcnt(0)
	v_mul_f32_e32 v57, v21, v61
	v_mul_f32_e32 v59, v19, v63
	v_fmac_f32_e32 v57, v20, v60
	v_fmac_f32_e32 v59, v18, v62
	v_add_f32_e32 v57, v57, v59
	v_add_f32_e32 v56, v56, v57
	v_mov_b32_e32 v57, v130
	ds_read_b128 v[60:63], v35 offset:40960
	v_add_f32_dpp v56, v56, v56 quad_perm:[1,0,3,2] row_mask:0xf bank_mask:0xf bound_ctrl:1
	s_nop 1
	v_add_f32_dpp v56, v56, v56 quad_perm:[2,3,0,1] row_mask:0xf bank_mask:0xf bound_ctrl:1
	s_nop 1
	v_add_f32_dpp v56, v56, v56 row_half_mirror row_mask:0xf bank_mask:0xf bound_ctrl:1
	s_nop 1
	v_add_f32_dpp v56, v56, v56 row_mirror row_mask:0xf bank_mask:0xf bound_ctrl:1
	s_nop 1
	v_mov_b32_dpp v57, v56 row_bcast:15 row_mask:0xa bank_mask:0xf
	v_add_f32_e32 v56, v56, v57
	v_mov_b32_e32 v57, v130
	s_nop 1
	v_mov_b32_dpp v57, v56 row_bcast:31 row_mask:0xc bank_mask:0xf
	v_add_f32_e32 v56, v56, v57
	s_waitcnt lgkmcnt(0)
	v_mul_f32_e32 v57, v45, v63
	v_readlane_b32 s2, v56, 63
	v_mul_f32_e32 v56, v47, v61
	v_fmac_f32_e32 v56, v46, v60
	v_fmac_f32_e32 v57, v44, v62
	ds_read_b128 v[60:63], v35 offset:40976
	v_add_f32_e32 v56, v56, v57
	v_add_f32_e32 v56, 0, v56
	s_waitcnt lgkmcnt(0)
	v_mul_f32_e32 v57, v55, v61
	v_mul_f32_e32 v59, v51, v63
	v_fmac_f32_e32 v57, v54, v60
	v_fmac_f32_e32 v59, v50, v62
	ds_read_b128 v[60:63], v35 offset:43008
	v_add_f32_e32 v57, v57, v59
	v_add_f32_e32 v56, v56, v57
	s_waitcnt lgkmcnt(0)
	v_mul_f32_e32 v57, v53, v61
	v_mul_f32_e32 v59, v49, v63
	v_fmac_f32_e32 v57, v52, v60
	v_fmac_f32_e32 v59, v48, v62
	ds_read_b128 v[60:63], v35 offset:43024
	v_add_f32_e32 v57, v57, v59
	v_add_f32_e32 v56, v56, v57
	s_waitcnt lgkmcnt(0)
	v_mul_f32_e32 v57, v33, v61
	v_mul_f32_e32 v59, v29, v63
	v_fmac_f32_e32 v57, v32, v60
	v_fmac_f32_e32 v59, v28, v62
	ds_read_b128 v[60:63], v35 offset:45056
	v_add_f32_e32 v57, v57, v59
	v_add_f32_e32 v56, v56, v57
	s_waitcnt lgkmcnt(0)
	v_mul_f32_e32 v57, v31, v61
	v_mul_f32_e32 v59, v27, v63
	v_fmac_f32_e32 v57, v30, v60
	v_fmac_f32_e32 v59, v26, v62
	ds_read_b128 v[60:63], v35 offset:45072
	v_add_f32_e32 v57, v57, v59
	v_add_f32_e32 v56, v56, v57
	s_waitcnt lgkmcnt(0)
	v_mul_f32_e32 v57, v25, v61
	v_mul_f32_e32 v59, v23, v63
	v_fmac_f32_e32 v57, v24, v60
	v_fmac_f32_e32 v59, v22, v62
	ds_read_b128 v[60:63], v35 offset:47104
	v_add_f32_e32 v57, v57, v59
	v_add_f32_e32 v56, v56, v57
	s_waitcnt lgkmcnt(0)
	v_mul_f32_e32 v57, v43, v61
	v_mul_f32_e32 v59, v41, v63
	v_fmac_f32_e32 v57, v42, v60
	v_fmac_f32_e32 v59, v40, v62
	ds_read_b128 v[60:63], v35 offset:47120
	v_add_f32_e32 v57, v57, v59
	v_add_f32_e32 v56, v56, v57
	s_waitcnt lgkmcnt(0)
	v_mul_f32_e32 v57, v21, v61
	v_mul_f32_e32 v59, v19, v63
	v_fmac_f32_e32 v57, v20, v60
	v_fmac_f32_e32 v59, v18, v62
	v_add_f32_e32 v57, v57, v59
	v_add_f32_e32 v56, v56, v57
	v_mov_b32_e32 v57, v130
	ds_read_b128 v[60:63], v35 offset:49152
	v_add_f32_dpp v56, v56, v56 quad_perm:[1,0,3,2] row_mask:0xf bank_mask:0xf bound_ctrl:1
	s_nop 1
	v_add_f32_dpp v56, v56, v56 quad_perm:[2,3,0,1] row_mask:0xf bank_mask:0xf bound_ctrl:1
	s_nop 1
	v_add_f32_dpp v56, v56, v56 row_half_mirror row_mask:0xf bank_mask:0xf bound_ctrl:1
	s_nop 1
	v_add_f32_dpp v56, v56, v56 row_mirror row_mask:0xf bank_mask:0xf bound_ctrl:1
	s_nop 1
	v_mov_b32_dpp v57, v56 row_bcast:15 row_mask:0xa bank_mask:0xf
	v_add_f32_e32 v56, v56, v57
	v_mov_b32_e32 v57, v130
	s_nop 1
	v_mov_b32_dpp v57, v56 row_bcast:31 row_mask:0xc bank_mask:0xf
	v_add_f32_e32 v56, v56, v57
	s_waitcnt lgkmcnt(0)
	v_mul_f32_e32 v57, v45, v63
	v_readlane_b32 s6, v56, 63
	v_mul_f32_e32 v56, v47, v61
	v_fmac_f32_e32 v56, v46, v60
	v_fmac_f32_e32 v57, v44, v62
	ds_read_b128 v[60:63], v35 offset:49168
	v_add_f32_e32 v56, v56, v57
	v_add_f32_e32 v56, 0, v56
	s_waitcnt lgkmcnt(0)
	v_mul_f32_e32 v57, v55, v61
	v_mul_f32_e32 v59, v51, v63
	v_fmac_f32_e32 v57, v54, v60
	v_fmac_f32_e32 v59, v50, v62
	ds_read_b128 v[60:63], v35 offset:51200
	v_add_f32_e32 v57, v57, v59
	v_add_f32_e32 v56, v56, v57
	s_waitcnt lgkmcnt(0)
	v_mul_f32_e32 v57, v53, v61
	v_mul_f32_e32 v59, v49, v63
	v_fmac_f32_e32 v57, v52, v60
	v_fmac_f32_e32 v59, v48, v62
	ds_read_b128 v[60:63], v35 offset:51216
	v_add_f32_e32 v57, v57, v59
	v_add_f32_e32 v56, v56, v57
	s_waitcnt lgkmcnt(0)
	v_mul_f32_e32 v57, v33, v61
	v_mul_f32_e32 v59, v29, v63
	v_fmac_f32_e32 v57, v32, v60
	v_fmac_f32_e32 v59, v28, v62
	ds_read_b128 v[60:63], v35 offset:53248
	v_add_f32_e32 v57, v57, v59
	v_add_f32_e32 v56, v56, v57
	s_waitcnt lgkmcnt(0)
	v_mul_f32_e32 v57, v31, v61
	v_mul_f32_e32 v59, v27, v63
	v_fmac_f32_e32 v57, v30, v60
	v_fmac_f32_e32 v59, v26, v62
	ds_read_b128 v[60:63], v35 offset:53264
	v_add_f32_e32 v57, v57, v59
	v_add_f32_e32 v56, v56, v57
	s_waitcnt lgkmcnt(0)
	v_mul_f32_e32 v57, v25, v61
	v_mul_f32_e32 v59, v23, v63
	v_fmac_f32_e32 v57, v24, v60
	v_fmac_f32_e32 v59, v22, v62
	ds_read_b128 v[60:63], v35 offset:55296
	v_add_f32_e32 v57, v57, v59
	v_add_f32_e32 v56, v56, v57
	s_waitcnt lgkmcnt(0)
	v_mul_f32_e32 v57, v43, v61
	v_mul_f32_e32 v59, v41, v63
	v_fmac_f32_e32 v57, v42, v60
	v_fmac_f32_e32 v59, v40, v62
	ds_read_b128 v[60:63], v35 offset:55312
	v_add_f32_e32 v57, v57, v59
	v_add_f32_e32 v56, v56, v57
	s_waitcnt lgkmcnt(0)
; #define LAS __attribute__((address_space(3)))
; template <int CTRL, int ROWMASK> __device__ __forceinline__ float dpp_f(float v) { return __int_as_float(__builtin_amdgcn_update_dpp(0, __float_as_int(v), CTRL, ROWMASK, 0xF, false)); }
; __device__ __forceinline__ float row16_sum(float v) { v += dpp_f<0xB1, 0xF>(v); v += dpp_f<0x4E, 0xF>(v); v += dpp_f<0x141, 0xF>(v); v += dpp_f<0x140, 0xF>(v); return v; }
; __device__ __forceinline__ float wave_sum(float v) {
;     v = row16_sum(v); v += dpp_f<0x142, 0xA>(v); v += dpp_f<0x143, 0xC>(v);
;     return __int_as_float(__builtin_amdgcn_readlane(__float_as_int(v), 63));
; }
; template <bool ROUTER, bool SMALLP>
; __device__ __forceinline__ void norm_phase(KA A, LAS unsigned char* lds, int l, int which, int npart, const float* pgate, int tid, int wave, int lane, int bid) {
;     ...
;             for (int e = 0; e < 8; ++e) { const LAS f32x4* wv = (const LAS f32x4*)(wrT + e * D) + 2 * lane; float a = 0.f;
; #pragma unroll
;                 for (int j = 0; j < 8; ++j) { const f32x4 w = wv[VIDX(j)]; a += (v[j].x * w.x + v[j].y * w.y) + (v[j].z * w.z + v[j].w * w.w); }
;                 lg[e] = wave_sum(a); }
	v_mul_f32_e32 v57, v21, v61
	v_mul_f32_e32 v59, v19, v63
	v_fmac_f32_e32 v57, v20, v60
	v_fmac_f32_e32 v59, v18, v62
	v_add_f32_e32 v57, v57, v59
	v_add_f32_e32 v56, v56, v57
	v_mov_b32_e32 v57, v130
	ds_read_b128 v[60:63], v35 offset:57344
	v_add_f32_dpp v56, v56, v56 quad_perm:[1,0,3,2] row_mask:0xf bank_mask:0xf bound_ctrl:1
	s_nop 1
	v_add_f32_dpp v56, v56, v56 quad_perm:[2,3,0,1] row_mask:0xf bank_mask:0xf bound_ctrl:1
	s_nop 1
	v_add_f32_dpp v56, v56, v56 row_half_mirror row_mask:0xf bank_mask:0xf bound_ctrl:1
	s_nop 1
	v_add_f32_dpp v56, v56, v56 row_mirror row_mask:0xf bank_mask:0xf bound_ctrl:1
	s_nop 1
	v_mov_b32_dpp v57, v56 row_bcast:15 row_mask:0xa bank_mask:0xf
	v_add_f32_e32 v56, v56, v57
	v_mov_b32_e32 v57, v130
	s_nop 1
	v_mov_b32_dpp v57, v56 row_bcast:31 row_mask:0xc bank_mask:0xf
	v_add_f32_e32 v56, v56, v57
	s_waitcnt lgkmcnt(0)
	v_mul_f32_e32 v57, v45, v63
	v_readlane_b32 s7, v56, 63
	v_mul_f32_e32 v56, v47, v61
	v_fmac_f32_e32 v56, v46, v60
	v_fmac_f32_e32 v57, v44, v62
	ds_read_b128 v[60:63], v35 offset:57360
	v_add_f32_e32 v56, v56, v57
	v_add_f32_e32 v56, 0, v56
	s_waitcnt lgkmcnt(0)
	v_mul_f32_e32 v57, v55, v61
	v_mul_f32_e32 v59, v51, v63
	v_fmac_f32_e32 v57, v54, v60
	v_fmac_f32_e32 v59, v50, v62
	ds_read_b128 v[60:63], v35 offset:59392
	v_add_f32_e32 v57, v57, v59
	v_add_f32_e32 v56, v56, v57
	s_waitcnt lgkmcnt(0)
	v_mul_f32_e32 v57, v53, v61
	v_mul_f32_e32 v59, v49, v63
	v_fmac_f32_e32 v57, v52, v60
	v_fmac_f32_e32 v59, v48, v62
	ds_read_b128 v[60:63], v35 offset:59408
	v_add_f32_e32 v57, v57, v59
	v_add_f32_e32 v56, v56, v57
	s_waitcnt lgkmcnt(0)
	v_mul_f32_e32 v57, v33, v61
	v_mul_f32_e32 v59, v29, v63
	v_fmac_f32_e32 v57, v32, v60
	v_fmac_f32_e32 v59, v28, v62
	ds_read_b128 v[60:63], v35 offset:61440
	v_add_f32_e32 v57, v57, v59
	v_add_f32_e32 v56, v56, v57
	s_waitcnt lgkmcnt(0)
	v_mul_f32_e32 v57, v31, v61
	v_mul_f32_e32 v59, v27, v63
	v_fmac_f32_e32 v57, v30, v60
	v_fmac_f32_e32 v59, v26, v62
	ds_read_b128 v[60:63], v35 offset:61456
	v_add_f32_e32 v57, v57, v59
	v_add_f32_e32 v56, v56, v57
	s_waitcnt lgkmcnt(0)
	v_mul_f32_e32 v57, v25, v61
	v_mul_f32_e32 v59, v23, v63
	v_fmac_f32_e32 v57, v24, v60
	v_fmac_f32_e32 v59, v22, v62
	ds_read_b128 v[60:63], v35 offset:63488
	v_add_f32_e32 v57, v57, v59
	v_add_f32_e32 v56, v56, v57
	s_waitcnt lgkmcnt(0)
	v_mul_f32_e32 v57, v43, v61
	v_mul_f32_e32 v59, v41, v63
	v_fmac_f32_e32 v57, v42, v60
	v_fmac_f32_e32 v59, v40, v62
	ds_read_b128 v[60:63], v35 offset:63504
	v_add_f32_e32 v57, v57, v59
	v_add_f32_e32 v56, v56, v57
	s_waitcnt lgkmcnt(0)
	v_mul_f32_e32 v57, v21, v61
	v_mul_f32_e32 v59, v19, v63
	v_fmac_f32_e32 v57, v20, v60
	v_fmac_f32_e32 v59, v18, v62
	v_add_f32_e32 v57, v57, v59
	v_add_f32_e32 v56, v56, v57
	v_mov_b32_e32 v57, v130
	ds_read_b128 v[60:63], v58 offset:32768
	ds_read_b128 v[64:67], v58 offset:32784
	v_add_f32_dpp v56, v56, v56 quad_perm:[1,0,3,2] row_mask:0xf bank_mask:0xf bound_ctrl:1
	s_waitcnt lgkmcnt(0)
	v_mul_f32_e32 v59, v51, v67
	v_add_f32_dpp v56, v56, v56 quad_perm:[2,3,0,1] row_mask:0xf bank_mask:0xf bound_ctrl:1
	v_fmac_f32_e32 v59, v50, v66
	s_nop 0
	v_add_f32_dpp v56, v56, v56 row_half_mirror row_mask:0xf bank_mask:0xf bound_ctrl:1
	s_nop 1
	v_add_f32_dpp v56, v56, v56 row_mirror row_mask:0xf bank_mask:0xf bound_ctrl:1
	s_nop 1
	v_mov_b32_dpp v57, v56 row_bcast:15 row_mask:0xa bank_mask:0xf
	v_add_f32_e32 v56, v56, v57
	v_mov_b32_e32 v57, v130
	s_nop 1
	v_mov_b32_dpp v57, v56 row_bcast:31 row_mask:0xc bank_mask:0xf
	v_add_f32_e32 v56, v56, v57
	v_mul_f32_e32 v57, v45, v63
	v_readlane_b32 s18, v56, 63
	v_mul_f32_e32 v56, v47, v61
	v_fmac_f32_e32 v56, v46, v60
	v_fmac_f32_e32 v57, v44, v62
	ds_read_b128 v[60:63], v58 offset:34816
	v_add_f32_e32 v56, v56, v57
	v_mul_f32_e32 v57, v55, v65
	v_fmac_f32_e32 v57, v54, v64
	v_add_f32_e32 v56, 0, v56
	v_add_f32_e32 v57, v57, v59
	v_add_f32_e32 v56, v56, v57
	s_waitcnt lgkmcnt(0)
	v_mul_f32_e32 v57, v53, v61
	v_mul_f32_e32 v59, v49, v63
	v_fmac_f32_e32 v57, v52, v60
	v_fmac_f32_e32 v59, v48, v62
	ds_read_b128 v[60:63], v58 offset:34832
	v_add_f32_e32 v57, v57, v59
	v_add_f32_e32 v56, v56, v57
	s_waitcnt lgkmcnt(0)
	v_mul_f32_e32 v57, v33, v61
	v_mul_f32_e32 v59, v29, v63
	v_fmac_f32_e32 v57, v32, v60
	v_fmac_f32_e32 v59, v28, v62
	ds_read_b128 v[60:63], v58 offset:36864
	v_add_f32_e32 v57, v57, v59
	v_add_f32_e32 v56, v56, v57
	s_waitcnt lgkmcnt(0)
	v_mul_f32_e32 v57, v31, v61
	v_mul_f32_e32 v59, v27, v63
	v_fmac_f32_e32 v57, v30, v60
	v_fmac_f32_e32 v59, v26, v62
	ds_read_b128 v[60:63], v58 offset:36880
	v_add_f32_e32 v57, v57, v59
	v_add_f32_e32 v56, v56, v57
	s_waitcnt lgkmcnt(0)
	v_mul_f32_e32 v57, v25, v61
	v_mul_f32_e32 v59, v23, v63
	v_fmac_f32_e32 v57, v24, v60
	v_fmac_f32_e32 v59, v22, v62
	ds_read_b128 v[60:63], v58 offset:38912
	v_add_f32_e32 v57, v57, v59
	v_add_f32_e32 v56, v56, v57
	s_waitcnt lgkmcnt(0)
	v_mul_f32_e32 v57, v43, v61
	v_mul_f32_e32 v59, v41, v63
	v_fmac_f32_e32 v57, v42, v60
	v_fmac_f32_e32 v59, v40, v62
	ds_read_b128 v[60:63], v58 offset:38928
	v_add_f32_e32 v57, v57, v59
	v_add_f32_e32 v56, v56, v57
	s_waitcnt lgkmcnt(0)
	v_mul_f32_e32 v57, v21, v61
	v_mul_f32_e32 v59, v19, v63
	v_fmac_f32_e32 v57, v20, v60
	v_fmac_f32_e32 v59, v18, v62
	v_add_f32_e32 v57, v57, v59
	v_add_f32_e32 v56, v56, v57
	v_mov_b32_e32 v57, v130
	ds_read_b128 v[60:63], v58 offset:40960
	v_add_f32_dpp v56, v56, v56 quad_perm:[1,0,3,2] row_mask:0xf bank_mask:0xf bound_ctrl:1
	s_nop 1
	v_add_f32_dpp v56, v56, v56 quad_perm:[2,3,0,1] row_mask:0xf bank_mask:0xf bound_ctrl:1
	s_nop 1
	v_add_f32_dpp v56, v56, v56 row_half_mirror row_mask:0xf bank_mask:0xf bound_ctrl:1
	s_nop 1
	v_add_f32_dpp v56, v56, v56 row_mirror row_mask:0xf bank_mask:0xf bound_ctrl:1
	s_nop 1
	v_mov_b32_dpp v57, v56 row_bcast:15 row_mask:0xa bank_mask:0xf
	v_add_f32_e32 v56, v56, v57
	v_mov_b32_e32 v57, v130
	s_nop 1
	v_mov_b32_dpp v57, v56 row_bcast:31 row_mask:0xc bank_mask:0xf
	v_add_f32_e32 v56, v56, v57
	s_waitcnt lgkmcnt(0)
; #define LAS __attribute__((address_space(3)))
; template <int CTRL, int ROWMASK> __device__ __forceinline__ float dpp_f(float v) { return __int_as_float(__builtin_amdgcn_update_dpp(0, __float_as_int(v), CTRL, ROWMASK, 0xF, false)); }
; __device__ __forceinline__ float row16_sum(float v) { v += dpp_f<0xB1, 0xF>(v); v += dpp_f<0x4E, 0xF>(v); v += dpp_f<0x141, 0xF>(v); v += dpp_f<0x140, 0xF>(v); return v; }
; __device__ __forceinline__ float wave_sum(float v) {
;     v = row16_sum(v); v += dpp_f<0x142, 0xA>(v); v += dpp_f<0x143, 0xC>(v);
;     return __int_as_float(__builtin_amdgcn_readlane(__float_as_int(v), 63));
; }
; template <bool ROUTER, bool SMALLP>
; __device__ __forceinline__ void norm_phase(KA A, LAS unsigned char* lds, int l, int which, int npart, const float* pgate, int tid, int wave, int lane, int bid) {
;     ...
;             for (int e = 0; e < 8; ++e) { const LAS f32x4* wv = (const LAS f32x4*)(wrT + e * D) + 2 * lane; float a = 0.f;
; #pragma unroll
;                 for (int j = 0; j < 8; ++j) { const f32x4 w = wv[VIDX(j)]; a += (v[j].x * w.x + v[j].y * w.y) + (v[j].z * w.z + v[j].w * w.w); }
;                 lg[e] = wave_sum(a); }
	v_mul_f32_e32 v57, v45, v63
	v_readlane_b32 s19, v56, 63
	v_mul_f32_e32 v56, v47, v61
	v_fmac_f32_e32 v56, v46, v60
	v_fmac_f32_e32 v57, v44, v62
	ds_read_b128 v[60:63], v58 offset:40976
	v_add_f32_e32 v56, v56, v57
	v_add_f32_e32 v56, 0, v56
	s_waitcnt lgkmcnt(0)
	v_mul_f32_e32 v57, v55, v61
	v_mul_f32_e32 v59, v51, v63
	v_fmac_f32_e32 v57, v54, v60
	v_fmac_f32_e32 v59, v50, v62
	ds_read_b128 v[60:63], v58 offset:43008
	v_add_f32_e32 v57, v57, v59
	v_add_f32_e32 v56, v56, v57
	s_waitcnt lgkmcnt(0)
	v_mul_f32_e32 v57, v53, v61
	v_mul_f32_e32 v59, v49, v63
	v_fmac_f32_e32 v57, v52, v60
	v_fmac_f32_e32 v59, v48, v62
	ds_read_b128 v[60:63], v58 offset:43024
	v_add_f32_e32 v57, v57, v59
	v_add_f32_e32 v56, v56, v57
	s_waitcnt lgkmcnt(0)
	v_mul_f32_e32 v57, v33, v61
	v_mul_f32_e32 v59, v29, v63
	v_fmac_f32_e32 v57, v32, v60
	v_fmac_f32_e32 v59, v28, v62
	ds_read_b128 v[60:63], v58 offset:45056
	v_add_f32_e32 v57, v57, v59
	v_add_f32_e32 v56, v56, v57
	s_waitcnt lgkmcnt(0)
	v_mul_f32_e32 v57, v31, v61
	v_mul_f32_e32 v59, v27, v63
	v_fmac_f32_e32 v57, v30, v60
	v_fmac_f32_e32 v59, v26, v62
	ds_read_b128 v[60:63], v58 offset:45072
	v_add_f32_e32 v57, v57, v59
	v_add_f32_e32 v56, v56, v57
	s_waitcnt lgkmcnt(0)
	v_mul_f32_e32 v57, v25, v61
	v_mul_f32_e32 v59, v23, v63
	v_fmac_f32_e32 v57, v24, v60
	v_fmac_f32_e32 v59, v22, v62
	ds_read_b128 v[60:63], v58 offset:47104
	v_add_f32_e32 v57, v57, v59
	v_add_f32_e32 v56, v56, v57
	s_waitcnt lgkmcnt(0)
	v_mul_f32_e32 v57, v43, v61
	v_mul_f32_e32 v59, v41, v63
	v_fmac_f32_e32 v57, v42, v60
	v_fmac_f32_e32 v59, v40, v62
	ds_read_b128 v[60:63], v58 offset:47120
	v_add_f32_e32 v57, v57, v59
	v_add_f32_e32 v56, v56, v57
	s_waitcnt lgkmcnt(0)
	v_mul_f32_e32 v57, v21, v61
	v_mul_f32_e32 v59, v19, v63
	v_fmac_f32_e32 v57, v20, v60
	v_fmac_f32_e32 v59, v18, v62
	v_add_f32_e32 v57, v57, v59
	v_add_f32_e32 v56, v56, v57
	v_mov_b32_e32 v57, v130
	ds_read_b128 v[60:63], v58 offset:49152
	v_add_f32_dpp v56, v56, v56 quad_perm:[1,0,3,2] row_mask:0xf bank_mask:0xf bound_ctrl:1
	s_nop 1
	v_add_f32_dpp v56, v56, v56 quad_perm:[2,3,0,1] row_mask:0xf bank_mask:0xf bound_ctrl:1
	s_nop 1
	v_add_f32_dpp v56, v56, v56 row_half_mirror row_mask:0xf bank_mask:0xf bound_ctrl:1
	s_nop 1
	v_add_f32_dpp v56, v56, v56 row_mirror row_mask:0xf bank_mask:0xf bound_ctrl:1
	s_nop 1
	v_mov_b32_dpp v57, v56 row_bcast:15 row_mask:0xa bank_mask:0xf
	v_add_f32_e32 v56, v56, v57
	v_mov_b32_e32 v57, v130
	s_nop 1
	v_mov_b32_dpp v57, v56 row_bcast:31 row_mask:0xc bank_mask:0xf
	v_add_f32_e32 v56, v56, v57
	s_waitcnt lgkmcnt(0)
	v_mul_f32_e32 v57, v45, v63
	v_readlane_b32 s20, v56, 63
	v_mul_f32_e32 v56, v47, v61
	v_fmac_f32_e32 v56, v46, v60
	v_fmac_f32_e32 v57, v44, v62
	ds_read_b128 v[60:63], v58 offset:49168
	v_add_f32_e32 v56, v56, v57
	v_add_f32_e32 v56, 0, v56
	s_waitcnt lgkmcnt(0)
	v_mul_f32_e32 v57, v55, v61
	v_mul_f32_e32 v59, v51, v63
	v_fmac_f32_e32 v57, v54, v60
	v_fmac_f32_e32 v59, v50, v62
	ds_read_b128 v[60:63], v58 offset:51200
	v_add_f32_e32 v57, v57, v59
	v_add_f32_e32 v56, v56, v57
	s_waitcnt lgkmcnt(0)
	v_mul_f32_e32 v57, v53, v61
	v_mul_f32_e32 v59, v49, v63
	v_fmac_f32_e32 v57, v52, v60
	v_fmac_f32_e32 v59, v48, v62
	ds_read_b128 v[60:63], v58 offset:51216
	v_add_f32_e32 v57, v57, v59
	v_add_f32_e32 v56, v56, v57
	s_waitcnt lgkmcnt(0)
	v_mul_f32_e32 v57, v33, v61
	v_mul_f32_e32 v59, v29, v63
	v_fmac_f32_e32 v57, v32, v60
	v_fmac_f32_e32 v59, v28, v62
	ds_read_b128 v[60:63], v58 offset:53248
	v_add_f32_e32 v57, v57, v59
	v_add_f32_e32 v56, v56, v57
	s_waitcnt lgkmcnt(0)
	v_mul_f32_e32 v57, v31, v61
	v_mul_f32_e32 v59, v27, v63
	v_fmac_f32_e32 v57, v30, v60
	v_fmac_f32_e32 v59, v26, v62
	ds_read_b128 v[60:63], v58 offset:53264
	v_add_f32_e32 v57, v57, v59
	v_add_f32_e32 v56, v56, v57
	s_waitcnt lgkmcnt(0)
	v_mul_f32_e32 v57, v25, v61
	v_mul_f32_e32 v59, v23, v63
	v_fmac_f32_e32 v57, v24, v60
	v_fmac_f32_e32 v59, v22, v62
	ds_read_b128 v[60:63], v58 offset:55296
	v_add_f32_e32 v57, v57, v59
	v_add_f32_e32 v56, v56, v57
	s_waitcnt lgkmcnt(0)
	v_mul_f32_e32 v57, v43, v61
	v_mul_f32_e32 v59, v41, v63
	v_fmac_f32_e32 v57, v42, v60
	v_fmac_f32_e32 v59, v40, v62
	ds_read_b128 v[60:63], v58 offset:55312
	v_add_f32_e32 v57, v57, v59
	v_add_f32_e32 v56, v56, v57
	s_waitcnt lgkmcnt(0)
	v_mul_f32_e32 v57, v21, v61
	v_mul_f32_e32 v59, v19, v63
	v_fmac_f32_e32 v57, v20, v60
	v_fmac_f32_e32 v59, v18, v62
	v_add_f32_e32 v57, v57, v59
	v_add_f32_e32 v56, v56, v57
	ds_read_b128 v[60:63], v58 offset:57344
	v_mov_b32_e32 v57, v130
	v_add_f32_dpp v56, v56, v56 quad_perm:[1,0,3,2] row_mask:0xf bank_mask:0xf bound_ctrl:1
	s_waitcnt lgkmcnt(0)
	v_mul_f32_e32 v47, v47, v61
	v_add_f32_dpp v56, v56, v56 quad_perm:[2,3,0,1] row_mask:0xf bank_mask:0xf bound_ctrl:1
	v_mul_f32_e32 v45, v45, v63
	v_fmac_f32_e32 v47, v46, v60
	v_add_f32_dpp v56, v56, v56 row_half_mirror row_mask:0xf bank_mask:0xf bound_ctrl:1
	v_fmac_f32_e32 v45, v44, v62
	v_add_f32_e32 v44, v47, v45
	v_add_f32_dpp v56, v56, v56 row_mirror row_mask:0xf bank_mask:0xf bound_ctrl:1
	s_nop 1
	v_mov_b32_dpp v57, v56 row_bcast:15 row_mask:0xa bank_mask:0xf
	v_add_f32_e32 v56, v56, v57
	v_mov_b32_e32 v57, v130
	s_nop 1
	v_mov_b32_dpp v57, v56 row_bcast:31 row_mask:0xc bank_mask:0xf
	v_add_f32_e32 v56, v56, v57
	s_nop 0
	v_readlane_b32 s22, v56, 63
	v_add_f32_e32 v56, 0, v44
	ds_read_b128 v[44:47], v58 offset:57360
	s_waitcnt lgkmcnt(0)
	v_mul_f32_e32 v45, v55, v45
	v_fmac_f32_e32 v45, v54, v44
	v_mul_f32_e32 v44, v51, v47
	v_fmac_f32_e32 v44, v50, v46
	v_add_f32_e32 v44, v45, v44
	v_add_f32_e32 v50, v56, v44
	ds_read_b128 v[44:47], v58 offset:59392
	s_waitcnt lgkmcnt(0)
; #define LAS __attribute__((address_space(3)))
; __device__ __forceinline__ unsigned long long rt() { return __builtin_amdgcn_s_memrealtime(); }
; template <bool ROUTER, bool SMALLP>
; __device__ __forceinline__ void norm_phase(KA A, LAS unsigned char* lds, int l, int which, int npart, const float* pgate, int tid, int wave, int lane, int bid) {
;     ...
;             for (int e = 0; e < 8; ++e) { const LAS f32x4* wv = (const LAS f32x4*)(wrT + e * D) + 2 * lane; float a = 0.f;
; #pragma unroll
;                 for (int j = 0; j < 8; ++j) { const f32x4 w = wv[VIDX(j)]; a += (v[j].x * w.x + v[j].y * w.y) + (v[j].z * w.z + v[j].w * w.w); }
;                 lg[e] = wave_sum(a); }
;             int e1 = 0; float v1 = lg[0];
; #pragma unroll
;             for (int e = 1; e < 8; ++e) if (lg[e] > v1) { v1 = lg[e]; e1 = e; }
;             int e2 = -1; float v2 = -3.0e38f;
; #pragma unroll
;             for (int e = 0; e < 8; ++e) if (e != e1 && lg[e] > v2) { v2 = lg[e]; e2 = e; }
;             const float ex = __expf(v2 - v1), w1 = 1.f / (1.f + ex), w2 = ex * w1;
;             if (lane == 0) { rt[rl * 4 + 0] = isctx ? -1 : e1; rt[rl * 4 + 1] = e2; rt[rl * 4 + 2] = __float_as_int(w1); rt[rl * 4 + 3] = __float_as_int(w2); }
	v_mul_f32_e32 v45, v53, v45
	v_fmac_f32_e32 v45, v52, v44
	v_mul_f32_e32 v44, v49, v47
	v_fmac_f32_e32 v44, v48, v46
	v_add_f32_e32 v44, v45, v44
	v_add_f32_e32 v48, v50, v44
	ds_read_b128 v[44:47], v58 offset:59408
	s_waitcnt lgkmcnt(0)
	v_mul_f32_e32 v33, v33, v45
	v_mul_f32_e32 v29, v29, v47
	v_fmac_f32_e32 v33, v32, v44
	v_fmac_f32_e32 v29, v28, v46
	ds_read_b128 v[44:47], v58 offset:61440
	v_add_f32_e32 v28, v33, v29
	v_add_f32_e32 v28, v48, v28
	s_waitcnt lgkmcnt(0)
	v_mul_f32_e32 v29, v31, v45
	v_mul_f32_e32 v27, v27, v47
	v_fmac_f32_e32 v29, v30, v44
	v_fmac_f32_e32 v27, v26, v46
	v_add_f32_e32 v26, v29, v27
	v_add_f32_e32 v30, v28, v26
	ds_read_b128 v[26:29], v58 offset:61456
	s_waitcnt lgkmcnt(0)
	v_mul_f32_e32 v25, v25, v27
	v_mul_f32_e32 v23, v23, v29
	v_fmac_f32_e32 v25, v24, v26
	v_fmac_f32_e32 v23, v22, v28
	v_add_f32_e32 v22, v25, v23
	v_add_f32_e32 v26, v30, v22
	ds_read_b128 v[22:25], v58 offset:63488
	s_waitcnt lgkmcnt(0)
	v_mul_f32_e32 v23, v43, v23
	v_fmac_f32_e32 v23, v42, v22
	v_mul_f32_e32 v22, v41, v25
	v_fmac_f32_e32 v22, v40, v24
	v_add_f32_e32 v22, v23, v22
	v_add_f32_e32 v26, v26, v22
	ds_read_b128 v[22:25], v58 offset:63504
	s_waitcnt lgkmcnt(0)
	v_mul_f32_e32 v21, v21, v23
	v_mul_f32_e32 v19, v19, v25
	v_fmac_f32_e32 v21, v20, v22
	v_fmac_f32_e32 v19, v18, v24
	v_add_f32_e32 v18, v21, v19
	v_add_f32_e32 v18, v26, v18
	v_mov_b32_e32 v19, v130
	s_nop 0
	v_add_f32_dpp v18, v18, v18 quad_perm:[1,0,3,2] row_mask:0xf bank_mask:0xf bound_ctrl:1
	s_nop 1
	v_add_f32_dpp v18, v18, v18 quad_perm:[2,3,0,1] row_mask:0xf bank_mask:0xf bound_ctrl:1
	s_nop 1
	v_add_f32_dpp v18, v18, v18 row_half_mirror row_mask:0xf bank_mask:0xf bound_ctrl:1
	s_nop 1
	v_add_f32_dpp v18, v18, v18 row_mirror row_mask:0xf bank_mask:0xf bound_ctrl:1
	s_nop 1
	v_mov_b32_dpp v19, v18 row_bcast:15 row_mask:0xa bank_mask:0xf
	v_add_f32_e32 v18, v18, v19
	v_mov_b32_e32 v19, v130
	s_nop 1
	v_mov_b32_dpp v19, v18 row_bcast:31 row_mask:0xc bank_mask:0xf
	v_add_f32_e32 v18, v18, v19
	s_nop 0
	v_readlane_b32 s23, v18, 63
	s_and_saveexec_b64 s[4:5], s[38:39]
	s_cbranch_execz .LBB0_1693
	v_mov_b32_e32 v18, s2
	v_cmp_gt_f32_e64 s[40:41], s6, v18
	v_mov_b32_e32 v19, s6
	v_mov_b32_e32 v21, s7
	v_cndmask_b32_e64 v20, v18, v19, s[40:41]
	v_cmp_gt_f32_e64 s[42:43], s7, v20
	v_mov_b32_e32 v22, s18
	v_mov_b32_e32 v23, s19
	v_cndmask_b32_e64 v20, v20, v21, s[42:43]
	v_cmp_gt_f32_e64 s[44:45], s18, v20
	v_mov_b32_e32 v24, s20
	v_mov_b32_e32 v25, s22
	v_cndmask_b32_e64 v20, v20, v22, s[44:45]
	v_cmp_gt_f32_e64 s[46:47], s19, v20
	v_cndmask_b32_e64 v26, 0, 1, s[40:41]
	s_nop 0
	v_cndmask_b32_e64 v20, v20, v23, s[46:47]
	v_cmp_gt_f32_e64 s[48:49], s20, v20
	v_readfirstlane_b32 s21, v26
	v_mov_b32_e32 v26, 0xff61b1e6
	v_cndmask_b32_e64 v20, v20, v24, s[48:49]
	v_cmp_gt_f32_e64 s[50:51], s22, v20
	v_cmp_ngt_f32_e64 s[40:41], s2, v26
	s_nop 0
	v_cndmask_b32_e64 v20, v20, v25, s[50:51]
	v_cmp_ngt_f32_e32 vcc, s23, v20
	s_and_b64 s[26:27], s[50:51], vcc
	s_and_b64 s[28:29], s[42:43], exec
	s_cselect_b32 s21, 2, s21
	s_and_b64 s[28:29], s[44:45], exec
	s_cselect_b32 s21, 3, s21
	s_and_b64 s[28:29], s[46:47], exec
	s_cselect_b32 s21, 4, s21
	s_and_b64 s[28:29], s[48:49], exec
	s_cselect_b32 s21, 5, s21
	s_and_b64 s[28:29], s[50:51], exec
	s_cselect_b32 s21, 6, s21
	s_and_b64 s[28:29], vcc, exec
	s_cselect_b32 s21, s21, 7
	s_cmp_lg_u32 s21, 5
	s_cselect_b64 s[28:29], -1, 0
	s_cmp_lg_u32 s21, 4
	s_cselect_b64 s[30:31], -1, 0
	s_cmp_lg_u32 s21, 3
	s_cselect_b64 s[36:37], -1, 0
	s_cmp_lg_u32 s21, 2
	s_cselect_b64 s[46:47], -1, 0
	s_cmp_lg_u32 s21, 1
	s_cselect_b64 s[44:45], -1, 0
	s_cmp_eq_u32 s21, 0
	s_cselect_b64 s[42:43], -1, 0
	s_or_b64 s[40:41], s[40:41], s[42:43]
	v_cndmask_b32_e64 v18, v18, v26, s[40:41]
	v_cmp_gt_f32_e64 s[42:43], s6, v18
	s_and_b64 s[42:43], s[44:45], s[42:43]
	s_nop 0
	v_cndmask_b32_e64 v18, v18, v19, s[42:43]
	v_cmp_gt_f32_e64 s[44:45], s7, v18
	s_and_b64 s[44:45], s[46:47], s[44:45]
	v_mov_b32_e32 v19, s23
	v_cndmask_b32_e64 v18, v18, v21, s[44:45]
	v_cmp_gt_f32_e64 s[46:47], s18, v18
	s_and_b64 s[46:47], s[36:37], s[46:47]
	v_cndmask_b32_e64 v21, 0, -1, s[40:41]
	v_cndmask_b32_e64 v18, v18, v22, s[46:47]
	v_cmp_gt_f32_e64 s[48:49], s19, v18
	s_and_b64 s[48:49], s[30:31], s[48:49]
	v_readfirstlane_b32 s2, v21
	v_cndmask_b32_e64 v18, v18, v23, s[48:49]
	v_cmp_gt_f32_e64 s[50:51], s20, v18
	s_and_b64 s[50:51], s[28:29], s[50:51]
	s_nop 0
	v_cndmask_b32_e64 v18, v18, v24, s[50:51]
	v_cmp_ngt_f32_e64 s[52:53], s22, v18
	s_or_b64 s[52:53], s[26:27], s[52:53]
	s_nop 0
	v_cndmask_b32_e64 v18, v25, v18, s[52:53]
	v_cmp_gt_f32_e64 s[54:55], s23, v18
	s_and_b64 s[54:55], vcc, s[54:55]
	s_and_b64 s[6:7], s[42:43], exec
	v_cndmask_b32_e64 v18, v18, v19, s[54:55]
	v_cndmask_b32_e32 v19, v19, v20, vcc
	v_sub_f32_e32 v18, v18, v19
	v_mul_f32_e32 v18, 0x3fb8aa3b, v18
	v_exp_f32_e32 v18, v18
	s_cselect_b32 s2, 1, s2
	s_and_b64 s[6:7], s[44:45], exec
	s_cselect_b32 s2, 2, s2
	v_add_f32_e32 v19, 1.0, v18
	v_div_scale_f32 v20, s[6:7], v19, v19, 1.0
	v_rcp_f32_e32 v21, v20
	s_and_b64 s[6:7], s[46:47], exec
	s_cselect_b32 s2, 3, s2
	s_and_b64 s[6:7], s[48:49], exec
	v_fma_f32 v22, -v20, v21, 1.0
	v_fmac_f32_e32 v21, v22, v21
	v_div_scale_f32 v22, vcc, 1.0, v19, 1.0
	v_mul_f32_e32 v23, v22, v21
	s_cselect_b32 s2, 4, s2
	s_and_b64 s[6:7], s[50:51], exec
	v_fma_f32 v24, -v20, v23, v22
	s_cselect_b32 s2, 5, s2
	s_and_b64 s[6:7], s[52:53], exec
	v_fmac_f32_e32 v23, v24, v21
	s_cselect_b32 s2, s2, 6
	s_and_b64 s[6:7], s[54:55], exec
	v_fma_f32 v20, -v20, v23, v22
	s_cselect_b32 s2, 7, s2
	v_div_fmas_f32 v20, v20, v21, v23
	s_and_b64 s[6:7], s[10:11], exec
	v_div_fixup_f32 v20, v20, v19, 1.0
	s_cselect_b32 s6, -1, s21
	s_add_i32 s7, s17, -12
	v_mul_f32_e32 v21, v18, v20
	v_mov_b32_e32 v18, s6
	v_mov_b32_e32 v19, s2
	v_mov_b32_e32 v22, s7
	ds_write_b128 v22, v[18:21]
	s_branch .LBB0_1693

;     __device__ __forceinline__ void operator()(const f32x16 (&acc)[2][2][2], const Unit& u, int wr, int wc, int c32, int h) const {
;         const int pl = u.pn % nt; const int row0 = u.pm * BM + wr * 64 + c32, col0 = pl * HALF + wc * 32 + 16 * h;
; #pragma unroll
;         for (int ai = 0; ai < 2; ++ai)
; #pragma unroll
;             for (int mb = 0; mb < 2; ++mb) { unsigned char* rowp = O + (size_t)(row0 + ai * HALF + mb * 32) * ldc + col0;
;                 float a[16];
; #pragma unroll
;                 for (int r = 0; r < 16; r += 2) {
;                     const f32x2 g = {acc[ai][0][mb][r], acc[ai][0][mb][r + 1]}, up = {acc[ai][1][mb][r], acc[ai][1][mb][r + 1]};
;                     const f32x2 x = g * (f32x2){-1.44269504f, -1.44269504f};
;                     const f32x2 d = (f32x2){__builtin_amdgcn_exp2f(x.x), __builtin_amdgcn_exp2f(x.y)} + (f32x2){1.f, 1.f};
;                     const f32x2 o = (g * up) * (f32x2){__builtin_amdgcn_rcpf(d.x), __builtin_amdgcn_rcpf(d.y)};
;                     a[r] = o.x; a[r + 1] = o.y; }
;                 u32x4 w; w.x = pk4_fp8(a[0], a[1], a[2], a[3]); w.y = pk4_fp8(a[4], a[5], a[6], a[7]); w.z = pk4_fp8(a[8], a[9], a[10], a[11]); w.w = pk4_fp8(a[12], a[13], a[14], a[15]);
;                 *(u32x4*)rowp = w; }
.LBB0_1899:
	s_mul_i32 s100, s30, 0x1c0000
	v_mov_b32_e32 v159, v153
	s_mov_b32 s30, 0xbfb8aa3b
	v_pk_mul_f32 v[160:161], v[98:99], s[30:31] op_sel_hi:[1,0]
	v_pk_mul_f32 v[116:117], v[100:101], v[116:117]
	v_exp_f32_e32 v160, v160
	v_exp_f32_e32 v161, v161
	v_pk_mul_f32 v[100:101], v[100:101], s[30:31] op_sel_hi:[1,0]
	v_pk_mul_f32 v[118:119], v[102:103], v[118:119]
	v_exp_f32_e32 v100, v100
	v_exp_f32_e32 v101, v101
	v_pk_add_f32 v[160:161], v[160:161], 1.0 op_sel_hi:[1,0]
	v_pk_mul_f32 v[102:103], v[102:103], s[30:31] op_sel_hi:[1,0]
	v_pk_mul_f32 v[98:99], v[98:99], v[114:115]
	v_rcp_f32_e32 v114, v160
	v_rcp_f32_e32 v115, v161
	v_pk_add_f32 v[100:101], v[100:101], 1.0 op_sel_hi:[1,0]
	v_exp_f32_e32 v102, v102
	v_exp_f32_e32 v103, v103
	v_rcp_f32_e32 v100, v100
	v_rcp_f32_e32 v101, v101
	v_pk_mul_f32 v[120:121], v[104:105], v[120:121]
	v_pk_mul_f32 v[104:105], v[104:105], s[30:31] op_sel_hi:[1,0]
	v_pk_mul_f32 v[122:123], v[106:107], v[122:123]
	v_pk_mul_f32 v[98:99], v[98:99], v[114:115]
	v_pk_add_f32 v[102:103], v[102:103], 1.0 op_sel_hi:[1,0]
	v_exp_f32_e32 v104, v104
	v_exp_f32_e32 v105, v105
	v_pk_mul_f32 v[106:107], v[106:107], s[30:31] op_sel_hi:[1,0]
	v_pk_mul_f32 v[100:101], v[116:117], v[100:101]
	v_rcp_f32_e32 v102, v102
	v_rcp_f32_e32 v103, v103
	v_exp_f32_e32 v106, v106
	v_exp_f32_e32 v107, v107
	v_med3_f32 v116, v98, s62, v236
	v_med3_f32 v99, v99, s62, v236
	v_cvt_pk_fp8_f32 v98, v116, v99
	v_pk_mul_f32 v[124:125], v[108:109], v[124:125]
	v_pk_add_f32 v[104:105], v[104:105], 1.0 op_sel_hi:[1,0]
	v_pk_mul_f32 v[108:109], v[108:109], s[30:31] op_sel_hi:[1,0]
	v_pk_mul_f32 v[126:127], v[110:111], v[126:127]
	v_pk_mul_f32 v[102:103], v[118:119], v[102:103]
	v_rcp_f32_e32 v104, v104
	v_rcp_f32_e32 v105, v105
	v_pk_add_f32 v[106:107], v[106:107], 1.0 op_sel_hi:[1,0]
	v_exp_f32_e32 v108, v108
	v_exp_f32_e32 v109, v109
	v_pk_mul_f32 v[110:111], v[110:111], s[30:31] op_sel_hi:[1,0]
	v_med3_f32 v100, v100, s62, v236
	v_med3_f32 v101, v101, s62, v236
	v_rcp_f32_e32 v106, v106
	v_rcp_f32_e32 v107, v107
	v_exp_f32_e32 v110, v110
	v_exp_f32_e32 v111, v111
	v_cvt_pk_fp8_f32 v98, v100, v101 op_sel:[0,0,1]
	v_med3_f32 v100, v102, s62, v236
	v_med3_f32 v101, v103, s62, v236
	v_cvt_pk_fp8_f32 v99, v100, v101
	v_pk_mul_f32 v[128:129], v[112:113], v[128:129]
	v_pk_mul_f32 v[104:105], v[120:121], v[104:105]
	v_pk_add_f32 v[108:109], v[108:109], 1.0 op_sel_hi:[1,0]
	v_pk_mul_f32 v[112:113], v[112:113], s[30:31] op_sel_hi:[1,0]
	v_pk_mul_f32 v[106:107], v[122:123], v[106:107]
	v_rcp_f32_e32 v108, v108
	v_rcp_f32_e32 v109, v109
	v_pk_add_f32 v[110:111], v[110:111], 1.0 op_sel_hi:[1,0]
	v_exp_f32_e32 v112, v112
	v_exp_f32_e32 v113, v113
	v_med3_f32 v102, v104, s62, v236
	v_med3_f32 v103, v105, s62, v236
	v_rcp_f32_e32 v110, v110
	v_rcp_f32_e32 v111, v111
	v_cvt_pk_fp8_f32 v99, v102, v103 op_sel:[0,0,1]
	v_med3_f32 v101, v106, s62, v236
	v_med3_f32 v102, v107, s62, v236
	v_cvt_pk_fp8_f32 v100, v101, v102
	v_pk_mul_f32 v[108:109], v[124:125], v[108:109]
	v_pk_add_f32 v[112:113], v[112:113], 1.0 op_sel_hi:[1,0]
	v_pk_mul_f32 v[110:111], v[126:127], v[110:111]
	v_rcp_f32_e32 v112, v112
	v_rcp_f32_e32 v113, v113
	v_med3_f32 v103, v108, s62, v236
	v_med3_f32 v104, v109, s62, v236
	s_mul_hi_i32 s6, s38, 0x92492493
	v_cvt_pk_fp8_f32 v100, v103, v104 op_sel:[0,0,1]
	v_med3_f32 v102, v110, s62, v236
	v_med3_f32 v103, v111, s62, v236
	v_mov_b32_e32 v101, v130
	s_add_i32 s6, s6, s38
	v_cvt_pk_fp8_f32 v101, v102, v103
	s_lshr_b32 s7, s6, 31
	s_lshr_b32 s6, s6, 5
	s_add_i32 s6, s6, s7
	v_pk_mul_f32 v[112:113], v[128:129], v[112:113]
	s_mul_i32 s6, s6, 56
	v_med3_f32 v104, v112, s62, v236
	v_med3_f32 v105, v113, s62, v236
	s_sub_i32 s6, s38, s6
	v_cvt_pk_fp8_f32 v101, v104, v105 op_sel:[0,0,1]
	s_lshl_b32 s101, s6, 15
	s_add_i32 s101, s101, s100
	v_add_u32_e32 v144, s101, v154
	v_mov_b64_e32 v[146:147], s[4:5]
	s_movk_i32 s15, 0x80
	v_ashrrev_i32_e32 v145, 31, v144
	v_mad_i64_i32 v[148:149], s[6:7], v159, s15, v[146:147]
	v_lshl_add_u64 v[114:115], v[148:149], 0, v[144:145]
	global_store_dwordx4 v[114:115], v[98:101], off
	v_pk_mul_f32 v[84:85], v[68:69], v[84:85]
	v_pk_mul_f32 v[68:69], v[68:69], s[30:31] op_sel_hi:[1,0]
	v_pk_mul_f32 v[100:101], v[66:67], s[30:31] op_sel_hi:[1,0]
	v_exp_f32_e32 v68, v68
	v_exp_f32_e32 v100, v100
	v_exp_f32_e32 v101, v101
	v_exp_f32_e32 v69, v69
	v_pk_mul_f32 v[86:87], v[70:71], v[86:87]
	v_pk_mul_f32 v[70:71], v[70:71], s[30:31] op_sel_hi:[1,0]
	v_pk_add_f32 v[100:101], v[100:101], 1.0 op_sel_hi:[1,0]
	v_pk_mul_f32 v[66:67], v[66:67], v[82:83]
	v_rcp_f32_e32 v82, v100
	v_rcp_f32_e32 v83, v101
	v_pk_add_f32 v[68:69], v[68:69], 1.0 op_sel_hi:[1,0]
	v_exp_f32_e32 v70, v70
	v_exp_f32_e32 v71, v71
	v_rcp_f32_e32 v68, v68
	v_rcp_f32_e32 v69, v69
	v_pk_mul_f32 v[88:89], v[72:73], v[88:89]
	v_pk_mul_f32 v[72:73], v[72:73], s[30:31] op_sel_hi:[1,0]
	v_pk_mul_f32 v[90:91], v[74:75], v[90:91]
	v_pk_mul_f32 v[66:67], v[66:67], v[82:83]
	v_pk_add_f32 v[70:71], v[70:71], 1.0 op_sel_hi:[1,0]
	v_exp_f32_e32 v72, v72
	v_exp_f32_e32 v73, v73
	v_pk_mul_f32 v[74:75], v[74:75], s[30:31] op_sel_hi:[1,0]
	v_pk_mul_f32 v[68:69], v[84:85], v[68:69]
	v_rcp_f32_e32 v70, v70
	v_rcp_f32_e32 v71, v71
	v_exp_f32_e32 v74, v74
	v_exp_f32_e32 v75, v75
	v_med3_f32 v84, v66, s62, v236
	v_med3_f32 v67, v67, s62, v236
	v_cvt_pk_fp8_f32 v66, v84, v67
	v_pk_mul_f32 v[92:93], v[76:77], v[92:93]
	v_pk_add_f32 v[72:73], v[72:73], 1.0 op_sel_hi:[1,0]
	v_pk_mul_f32 v[76:77], v[76:77], s[30:31] op_sel_hi:[1,0]
	v_pk_mul_f32 v[94:95], v[78:79], v[94:95]
	v_pk_mul_f32 v[70:71], v[86:87], v[70:71]
	v_rcp_f32_e32 v72, v72
	v_rcp_f32_e32 v73, v73
;     __device__ __forceinline__ void operator()(const f32x16 (&acc)[2][2][2], const Unit& u, int wr, int wc, int c32, int h) const {
;         const int pl = u.pn % nt; const int row0 = u.pm * BM + wr * 64 + c32, col0 = pl * HALF + wc * 32 + 16 * h;
; #pragma unroll
;         for (int ai = 0; ai < 2; ++ai)
; #pragma unroll
;             for (int mb = 0; mb < 2; ++mb) { unsigned char* rowp = O + (size_t)(row0 + ai * HALF + mb * 32) * ldc + col0;
;                 float a[16];
; #pragma unroll
;                 for (int r = 0; r < 16; r += 2) {
;                     const f32x2 g = {acc[ai][0][mb][r], acc[ai][0][mb][r + 1]}, up = {acc[ai][1][mb][r], acc[ai][1][mb][r + 1]};
;                     const f32x2 x = g * (f32x2){-1.44269504f, -1.44269504f};
;                     const f32x2 d = (f32x2){__builtin_amdgcn_exp2f(x.x), __builtin_amdgcn_exp2f(x.y)} + (f32x2){1.f, 1.f};
;                     const f32x2 o = (g * up) * (f32x2){__builtin_amdgcn_rcpf(d.x), __builtin_amdgcn_rcpf(d.y)};
;                     a[r] = o.x; a[r + 1] = o.y; }
;                 u32x4 w; w.x = pk4_fp8(a[0], a[1], a[2], a[3]); w.y = pk4_fp8(a[4], a[5], a[6], a[7]); w.z = pk4_fp8(a[8], a[9], a[10], a[11]); w.w = pk4_fp8(a[12], a[13], a[14], a[15]);
;                 *(u32x4*)rowp = w; }
	v_pk_add_f32 v[74:75], v[74:75], 1.0 op_sel_hi:[1,0]
	v_exp_f32_e32 v76, v76
	v_exp_f32_e32 v77, v77
	v_pk_mul_f32 v[78:79], v[78:79], s[30:31] op_sel_hi:[1,0]
	v_med3_f32 v68, v68, s62, v236
	v_med3_f32 v69, v69, s62, v236
	v_rcp_f32_e32 v74, v74
	v_rcp_f32_e32 v75, v75
	v_exp_f32_e32 v78, v78
	v_exp_f32_e32 v79, v79
	v_cvt_pk_fp8_f32 v66, v68, v69 op_sel:[0,0,1]
	v_med3_f32 v68, v70, s62, v236
	v_med3_f32 v69, v71, s62, v236
	v_cvt_pk_fp8_f32 v67, v68, v69
	v_pk_mul_f32 v[96:97], v[80:81], v[96:97]
	v_pk_mul_f32 v[72:73], v[88:89], v[72:73]
	v_pk_add_f32 v[76:77], v[76:77], 1.0 op_sel_hi:[1,0]
	v_pk_mul_f32 v[80:81], v[80:81], s[30:31] op_sel_hi:[1,0]
	v_pk_mul_f32 v[74:75], v[90:91], v[74:75]
	v_rcp_f32_e32 v76, v76
	v_rcp_f32_e32 v77, v77
	v_pk_add_f32 v[78:79], v[78:79], 1.0 op_sel_hi:[1,0]
	v_exp_f32_e32 v80, v80
	v_exp_f32_e32 v81, v81
	v_med3_f32 v70, v72, s62, v236
	v_med3_f32 v71, v73, s62, v236
	v_rcp_f32_e32 v78, v78
	v_rcp_f32_e32 v79, v79
	v_cvt_pk_fp8_f32 v67, v70, v71 op_sel:[0,0,1]
	v_med3_f32 v69, v74, s62, v236
	v_med3_f32 v70, v75, s62, v236
	v_cvt_pk_fp8_f32 v68, v69, v70
	v_pk_mul_f32 v[76:77], v[92:93], v[76:77]
	v_pk_add_f32 v[80:81], v[80:81], 1.0 op_sel_hi:[1,0]
	v_pk_mul_f32 v[78:79], v[94:95], v[78:79]
	v_rcp_f32_e32 v80, v80
	v_rcp_f32_e32 v81, v81
	v_med3_f32 v71, v76, s62, v236
	v_med3_f32 v72, v77, s62, v236
	v_cvt_pk_fp8_f32 v68, v71, v72 op_sel:[0,0,1]
	v_med3_f32 v70, v78, s62, v236
	v_med3_f32 v71, v79, s62, v236
	v_cvt_pk_fp8_f32 v69, v70, v71
	v_pk_mul_f32 v[80:81], v[96:97], v[80:81]
	v_or_b32_e32 v98, 32, v159
	v_med3_f32 v72, v80, s62, v236
	v_med3_f32 v73, v81, s62, v236
	v_cvt_pk_fp8_f32 v69, v72, v73 op_sel:[0,0,1]
	v_mad_i64_i32 v[98:99], s[6:7], v98, s15, v[146:147]
	v_lshl_add_u64 v[82:83], v[98:99], 0, v[144:145]
	global_store_dwordx4 v[82:83], v[66:69], off
	v_pk_mul_f32 v[52:53], v[36:37], v[52:53]
	v_pk_mul_f32 v[36:37], v[36:37], s[30:31] op_sel_hi:[1,0]
	v_pk_mul_f32 v[68:69], v[34:35], s[30:31] op_sel_hi:[1,0]
	v_exp_f32_e32 v36, v36
	v_exp_f32_e32 v68, v68
	v_exp_f32_e32 v69, v69
	v_exp_f32_e32 v37, v37
	v_pk_mul_f32 v[54:55], v[38:39], v[54:55]
	v_pk_mul_f32 v[38:39], v[38:39], s[30:31] op_sel_hi:[1,0]
	v_pk_add_f32 v[68:69], v[68:69], 1.0 op_sel_hi:[1,0]
	v_pk_mul_f32 v[34:35], v[34:35], v[50:51]
	v_rcp_f32_e32 v50, v68
	v_rcp_f32_e32 v51, v69
	v_pk_add_f32 v[36:37], v[36:37], 1.0 op_sel_hi:[1,0]
	v_exp_f32_e32 v38, v38
	v_exp_f32_e32 v39, v39
	v_rcp_f32_e32 v36, v36
	v_rcp_f32_e32 v37, v37
	v_pk_mul_f32 v[56:57], v[40:41], v[56:57]
	v_pk_mul_f32 v[40:41], v[40:41], s[30:31] op_sel_hi:[1,0]
	v_pk_mul_f32 v[58:59], v[42:43], v[58:59]
	v_pk_mul_f32 v[34:35], v[34:35], v[50:51]
	v_pk_add_f32 v[38:39], v[38:39], 1.0 op_sel_hi:[1,0]
	v_exp_f32_e32 v40, v40
	v_exp_f32_e32 v41, v41
	v_pk_mul_f32 v[42:43], v[42:43], s[30:31] op_sel_hi:[1,0]
	v_pk_mul_f32 v[36:37], v[52:53], v[36:37]
	v_rcp_f32_e32 v38, v38
	v_rcp_f32_e32 v39, v39
	v_exp_f32_e32 v42, v42
	v_exp_f32_e32 v43, v43
	v_med3_f32 v52, v34, s62, v236
	v_med3_f32 v35, v35, s62, v236
	v_cvt_pk_fp8_f32 v34, v52, v35
	v_pk_mul_f32 v[60:61], v[44:45], v[60:61]
	v_pk_add_f32 v[40:41], v[40:41], 1.0 op_sel_hi:[1,0]
	v_pk_mul_f32 v[44:45], v[44:45], s[30:31] op_sel_hi:[1,0]
	v_pk_mul_f32 v[62:63], v[46:47], v[62:63]
	v_pk_mul_f32 v[38:39], v[54:55], v[38:39]
	v_rcp_f32_e32 v40, v40
	v_rcp_f32_e32 v41, v41
	v_pk_add_f32 v[42:43], v[42:43], 1.0 op_sel_hi:[1,0]
	v_exp_f32_e32 v44, v44
	v_exp_f32_e32 v45, v45
	v_pk_mul_f32 v[46:47], v[46:47], s[30:31] op_sel_hi:[1,0]
	v_med3_f32 v36, v36, s62, v236
	v_med3_f32 v37, v37, s62, v236
	v_rcp_f32_e32 v42, v42
	v_rcp_f32_e32 v43, v43
	v_exp_f32_e32 v46, v46
	v_exp_f32_e32 v47, v47
	v_cvt_pk_fp8_f32 v34, v36, v37 op_sel:[0,0,1]
	v_med3_f32 v36, v38, s62, v236
	v_med3_f32 v37, v39, s62, v236
	v_cvt_pk_fp8_f32 v35, v36, v37
	v_pk_mul_f32 v[64:65], v[48:49], v[64:65]
	v_pk_mul_f32 v[40:41], v[56:57], v[40:41]
	v_pk_add_f32 v[44:45], v[44:45], 1.0 op_sel_hi:[1,0]
	v_pk_mul_f32 v[48:49], v[48:49], s[30:31] op_sel_hi:[1,0]
	v_pk_mul_f32 v[42:43], v[58:59], v[42:43]
	v_rcp_f32_e32 v44, v44
	v_rcp_f32_e32 v45, v45
	v_pk_add_f32 v[46:47], v[46:47], 1.0 op_sel_hi:[1,0]
	v_exp_f32_e32 v48, v48
	v_exp_f32_e32 v49, v49
	v_med3_f32 v38, v40, s62, v236
	v_med3_f32 v39, v41, s62, v236
	v_rcp_f32_e32 v46, v46
	v_rcp_f32_e32 v47, v47
;     __device__ __forceinline__ void done(const Unit&, int ui, PG8_LAS unsigned char* lds, int tid) const { if constexpr (HOOK) { if (ui == cv.trig) conv_burst<4, true>(cv, c, lds + 131072, tid); } }
;     __device__ __forceinline__ void done(const Unit&, int ui, PG8_LAS unsigned char* lds, int tid) const { if constexpr (HOOK) { if (ui == cv.trig) conv_burst<4, true>(cv, c, lds + 131072, tid); } }
; #define PG8_BAR __builtin_amdgcn_s_barrier()
; #define PG8_BAR __builtin_amdgcn_s_barrier()
; #define PG8_ZERO() do { _Pragma("unroll") for (int a = 0; a < 2; ++a) _Pragma("unroll") for (int b = 0; b < 2; ++b) _Pragma("unroll") for (int m = 0; m < 2; ++m) _Pragma("unroll") for (int e = 0; e < 16; ++e) acc[a][b][m][e] = 0.f; } while (0)
; template <class Epi, class Sched, int SCW, int SCX, int SCW1 = SCW>
; __device__ __forceinline__ void gemm_phase_f8(PG8_LAS unsigned char* lds, const Gemm g, const Sched& S, const Epi& E, const int tid) {
;     ...
;         if (wr == 0) PG8_BAR;
;         E(acc, cur, wr, wc, r32, kh); S.done(cur, ui, lds, tid);
;         if (!has_next) break;
;         PG8_ZERO();
;         cur = nxt; cA = nA; cB = nB; ++ui; nt = cur.nt;
;         if (wr == 1) PG8_BAR;
;     __device__ __forceinline__ void operator()(const f32x16 (&acc)[2][2][2], const Unit& u, int wr, int wc, int c32, int h) const {
;     ...
;         for (int ai = 0; ai < 2; ++ai)
; #pragma unroll
;             for (int mb = 0; mb < 2; ++mb) { unsigned char* rowp = O + (size_t)(row0 + ai * HALF + mb * 32) * ldc + col0;
;                 float a[16];
; #pragma unroll
;                 for (int r = 0; r < 16; r += 2) {
;                     const f32x2 g = {acc[ai][0][mb][r], acc[ai][0][mb][r + 1]}, up = {acc[ai][1][mb][r], acc[ai][1][mb][r + 1]};
;                     const f32x2 x = g * (f32x2){-1.44269504f, -1.44269504f};
;                     const f32x2 d = (f32x2){__builtin_amdgcn_exp2f(x.x), __builtin_amdgcn_exp2f(x.y)} + (f32x2){1.f, 1.f};
;                     const f32x2 o = (g * up) * (f32x2){__builtin_amdgcn_rcpf(d.x), __builtin_amdgcn_rcpf(d.y)};
;                     a[r] = o.x; a[r + 1] = o.y; }
;                 u32x4 w; w.x = pk4_fp8(a[0], a[1], a[2], a[3]); w.y = pk4_fp8(a[4], a[5], a[6], a[7]); w.z = pk4_fp8(a[8], a[9], a[10], a[11]); w.w = pk4_fp8(a[12], a[13], a[14], a[15]);
;                 *(u32x4*)rowp = w; }
	v_cvt_pk_fp8_f32 v35, v38, v39 op_sel:[0,0,1]
	v_med3_f32 v37, v42, s62, v236
	v_med3_f32 v38, v43, s62, v236
	v_cvt_pk_fp8_f32 v36, v37, v38
	v_pk_mul_f32 v[44:45], v[60:61], v[44:45]
	v_pk_add_f32 v[48:49], v[48:49], 1.0 op_sel_hi:[1,0]
	v_pk_mul_f32 v[46:47], v[62:63], v[46:47]
	v_rcp_f32_e32 v48, v48
	v_rcp_f32_e32 v49, v49
	v_med3_f32 v39, v44, s62, v236
	v_med3_f32 v40, v45, s62, v236
	v_cvt_pk_fp8_f32 v36, v39, v40 op_sel:[0,0,1]
	v_med3_f32 v38, v46, s62, v236
	v_med3_f32 v39, v47, s62, v236
	v_cvt_pk_fp8_f32 v37, v38, v39
	v_pk_mul_f32 v[48:49], v[64:65], v[48:49]
	v_add_u32_e32 v66, 0x80, v159
	v_med3_f32 v40, v48, s62, v236
	v_med3_f32 v41, v49, s62, v236
	v_cvt_pk_fp8_f32 v37, v40, v41 op_sel:[0,0,1]
	v_mad_i64_i32 v[66:67], s[6:7], v66, s15, v[146:147]
	v_lshl_add_u64 v[50:51], v[66:67], 0, v[144:145]
	global_store_dwordx4 v[50:51], v[34:37], off
	v_pk_mul_f32 v[20:21], v[4:5], v[20:21]
	v_pk_mul_f32 v[4:5], v[4:5], s[30:31] op_sel_hi:[1,0]
	v_pk_mul_f32 v[36:37], v[2:3], s[30:31] op_sel_hi:[1,0]
	v_exp_f32_e32 v4, v4
	v_exp_f32_e32 v36, v36
	v_exp_f32_e32 v37, v37
	v_exp_f32_e32 v5, v5
	v_pk_mul_f32 v[22:23], v[6:7], v[22:23]
	v_pk_mul_f32 v[6:7], v[6:7], s[30:31] op_sel_hi:[1,0]
	v_pk_add_f32 v[36:37], v[36:37], 1.0 op_sel_hi:[1,0]
	v_pk_mul_f32 v[2:3], v[2:3], v[18:19]
	v_rcp_f32_e32 v18, v36
	v_rcp_f32_e32 v19, v37
	v_pk_add_f32 v[4:5], v[4:5], 1.0 op_sel_hi:[1,0]
	v_exp_f32_e32 v6, v6
	v_exp_f32_e32 v7, v7
	v_rcp_f32_e32 v4, v4
	v_rcp_f32_e32 v5, v5
	v_pk_mul_f32 v[24:25], v[8:9], v[24:25]
	v_pk_mul_f32 v[8:9], v[8:9], s[30:31] op_sel_hi:[1,0]
	v_pk_mul_f32 v[26:27], v[10:11], v[26:27]
	v_pk_mul_f32 v[2:3], v[2:3], v[18:19]
	v_pk_add_f32 v[6:7], v[6:7], 1.0 op_sel_hi:[1,0]
	v_exp_f32_e32 v8, v8
	v_exp_f32_e32 v9, v9
	v_pk_mul_f32 v[10:11], v[10:11], s[30:31] op_sel_hi:[1,0]
	v_pk_mul_f32 v[4:5], v[20:21], v[4:5]
	v_rcp_f32_e32 v6, v6
	v_rcp_f32_e32 v7, v7
	v_exp_f32_e32 v10, v10
	v_exp_f32_e32 v11, v11
	v_med3_f32 v20, v2, s62, v236
	v_med3_f32 v3, v3, s62, v236
	v_cvt_pk_fp8_f32 v2, v20, v3
	v_pk_mul_f32 v[28:29], v[12:13], v[28:29]
	v_pk_add_f32 v[8:9], v[8:9], 1.0 op_sel_hi:[1,0]
	v_pk_mul_f32 v[12:13], v[12:13], s[30:31] op_sel_hi:[1,0]
	v_pk_mul_f32 v[30:31], v[14:15], v[30:31]
	v_pk_mul_f32 v[6:7], v[22:23], v[6:7]
	v_rcp_f32_e32 v8, v8
	v_rcp_f32_e32 v9, v9
	v_pk_add_f32 v[10:11], v[10:11], 1.0 op_sel_hi:[1,0]
	v_exp_f32_e32 v12, v12
	v_exp_f32_e32 v13, v13
	v_pk_mul_f32 v[14:15], v[14:15], s[30:31] op_sel_hi:[1,0]
	v_med3_f32 v4, v4, s62, v236
	v_med3_f32 v5, v5, s62, v236
	v_rcp_f32_e32 v10, v10
	v_rcp_f32_e32 v11, v11
	v_exp_f32_e32 v14, v14
	v_exp_f32_e32 v15, v15
	v_cvt_pk_fp8_f32 v2, v4, v5 op_sel:[0,0,1]
	v_med3_f32 v4, v6, s62, v236
	v_med3_f32 v5, v7, s62, v236
	v_cvt_pk_fp8_f32 v3, v4, v5
	v_pk_mul_f32 v[32:33], v[16:17], v[32:33]
	v_pk_mul_f32 v[8:9], v[24:25], v[8:9]
	v_pk_add_f32 v[12:13], v[12:13], 1.0 op_sel_hi:[1,0]
	v_pk_mul_f32 v[16:17], v[16:17], s[30:31] op_sel_hi:[1,0]
	v_pk_mul_f32 v[10:11], v[26:27], v[10:11]
	v_rcp_f32_e32 v12, v12
	v_rcp_f32_e32 v13, v13
	v_pk_add_f32 v[14:15], v[14:15], 1.0 op_sel_hi:[1,0]
	v_exp_f32_e32 v16, v16
	v_exp_f32_e32 v17, v17
	v_med3_f32 v6, v8, s62, v236
	v_med3_f32 v7, v9, s62, v236
	v_rcp_f32_e32 v14, v14
	v_rcp_f32_e32 v15, v15
	v_cvt_pk_fp8_f32 v3, v6, v7 op_sel:[0,0,1]
	v_med3_f32 v5, v10, s62, v236
	v_med3_f32 v6, v11, s62, v236
	v_cvt_pk_fp8_f32 v4, v5, v6
	v_pk_mul_f32 v[12:13], v[28:29], v[12:13]
	v_pk_add_f32 v[16:17], v[16:17], 1.0 op_sel_hi:[1,0]
	v_pk_mul_f32 v[14:15], v[30:31], v[14:15]
	v_rcp_f32_e32 v16, v16
	v_rcp_f32_e32 v17, v17
	v_med3_f32 v7, v12, s62, v236
	v_med3_f32 v8, v13, s62, v236
	v_cvt_pk_fp8_f32 v4, v7, v8 op_sel:[0,0,1]
	v_med3_f32 v6, v14, s62, v236
	v_med3_f32 v7, v15, s62, v236
	v_cvt_pk_fp8_f32 v5, v6, v7
	v_pk_mul_f32 v[16:17], v[32:33], v[16:17]
	v_add_u32_e32 v34, 0xa0, v159
	v_med3_f32 v8, v16, s62, v236
	v_med3_f32 v9, v17, s62, v236
	v_cvt_pk_fp8_f32 v5, v8, v9 op_sel:[0,0,1]
	v_mad_i64_i32 v[34:35], s[6:7], v34, s15, v[146:147]
	v_lshl_add_u64 v[18:19], v[34:35], 0, v[144:145]
	s_mov_b64 s[6:7], -1
	s_andn2_b64 vcc, exec, s[10:11]
	s_movk_i32 s63, 0xd0
	s_movk_i32 s66, 0x2c00
	s_movk_i32 s67, 0x104
	global_store_dwordx4 v[18:19], v[2:5], off
	s_cbranch_vccnz .LBB0_1892
	s_andn2_b64 vcc, exec, s[0:1]
	s_cbranch_vccnz .LBB0_1891
	s_barrier
	s_branch .LBB0_1891

; #define GAS __attribute__((address_space(1)))
; #define LAS __attribute__((address_space(3)))
; #define LDS_BARRIER() do { asm volatile("s_waitcnt lgkmcnt(0)" ::: "memory"); __builtin_amdgcn_s_barrier(); asm volatile("" ::: "memory"); } while (0)
; template <class RowMap>
; __device__ __forceinline__ void conv_store_fp8(const f32x4 (&r)[8], unsigned char* WT, int Kbytes, int k0bytes, int n0, const RowMap rm, LAS unsigned char* T, int tid, int wave, int lane) {
;     ...
;     for (int j = 0; j < 4; ++j) { const unsigned lo = pk4_fp8(r[0][j] * W8_SCALE, r[1][j] * W8_SCALE, r[2][j] * W8_SCALE, r[3][j] * W8_SCALE), hi = pk4_fp8(r[4][j] * W8_SCALE, r[5][j] * W8_SCALE, r[6][j] * W8_SCALE, r[7][j] * W8_SCALE);
;         *(LAS unsigned long long*)(T + (4 * lane + j) * 64 + 8 * (wave ^ s)) = (unsigned long long)lo | ((unsigned long long)hi << 32); }
;     LDS_BARRIER();
;     const int c16 = tid & 3, rr = tid >> 2;
; #pragma unroll
;     for (int q = 0; q < 2; ++q) { const int row = rr + 128 * q; const v4u v = *(const LAS v4u*)(T + row * 64 + 16 * (c16 ^ ((row >> 2) & 3)));
;         const int dr = rm(n0 + row); if (dr >= 0) *(GAS v4u*)(WT + (unsigned)((((dr >> 8) * (Kbytes >> 7) + (k0bytes >> 7)) << 15) + ((dr & 255) << 7) + (k0bytes & 127) + 16 * c16)) = v; }
.Lhw_done_7:
	v_med3_f32 v131, v2, s101, v200
	v_med3_f32 v153, v6, s101, v200
	v_cvt_scalef32_pk_fp8_f32 v132, v131, v153, v201
	v_med3_f32 v133, v10, s101, v200
	v_med3_f32 v152, v14, s101, v200
	v_cvt_scalef32_pk_fp8_f32 v132, v133, v152, v201 op_sel:[0,0,0,1]
	v_med3_f32 v131, v18, s101, v200
	v_med3_f32 v158, v22, s101, v200
	v_cvt_scalef32_pk_fp8_f32 v133, v131, v158, v201
	v_med3_f32 v152, v50, s101, v200
	v_med3_f32 v153, v54, s101, v200
	v_cvt_scalef32_pk_fp8_f32 v133, v152, v153, v201 op_sel:[0,0,0,1]
	v_med3_f32 v131, v3, s101, v200
	v_med3_f32 v159, v7, s101, v200
	v_cvt_scalef32_pk_fp8_f32 v152, v131, v159, v201
	v_med3_f32 v153, v11, s101, v200
	v_med3_f32 v158, v15, s101, v200
	v_cvt_scalef32_pk_fp8_f32 v152, v153, v158, v201 op_sel:[0,0,0,1]
	v_med3_f32 v131, v19, s101, v200
	v_med3_f32 v172, v23, s101, v200
	v_cvt_scalef32_pk_fp8_f32 v153, v131, v172, v201
	v_med3_f32 v158, v51, s101, v200
	v_med3_f32 v159, v55, s101, v200
	v_cvt_scalef32_pk_fp8_f32 v153, v158, v159, v201 op_sel:[0,0,0,1]
	v_med3_f32 v131, v4, s101, v200
	s_cmp_lg_u32 s12, 0
	ds_write2_b64 v171, v[132:133], v[152:153] offset1:8
	v_med3_f32 v153, v8, s101, v200
	v_cvt_scalef32_pk_fp8_f32 v132, v131, v153, v201
	v_med3_f32 v133, v12, s101, v200
	v_med3_f32 v152, v16, s101, v200
	v_cvt_scalef32_pk_fp8_f32 v132, v133, v152, v201 op_sel:[0,0,0,1]
	v_med3_f32 v131, v20, s101, v200
	v_med3_f32 v158, v24, s101, v200
	v_cvt_scalef32_pk_fp8_f32 v133, v131, v158, v201
	v_med3_f32 v152, v52, s101, v200
	v_med3_f32 v153, v56, s101, v200
	v_cvt_scalef32_pk_fp8_f32 v133, v152, v153, v201 op_sel:[0,0,0,1]
	v_med3_f32 v131, v5, s101, v200
	v_med3_f32 v159, v9, s101, v200
	v_cvt_scalef32_pk_fp8_f32 v152, v131, v159, v201
	v_med3_f32 v153, v13, s101, v200
	v_med3_f32 v158, v17, s101, v200
	v_cvt_scalef32_pk_fp8_f32 v152, v153, v158, v201 op_sel:[0,0,0,1]
	v_med3_f32 v131, v21, s101, v200
	v_med3_f32 v172, v25, s101, v200
	v_cvt_scalef32_pk_fp8_f32 v153, v131, v172, v201
	v_med3_f32 v158, v53, s101, v200
	v_med3_f32 v159, v57, s101, v200
	v_cvt_scalef32_pk_fp8_f32 v153, v158, v159, v201 op_sel:[0,0,0,1]
	ds_write2_b64 v171, v[132:133], v[152:153] offset0:16 offset1:24
	s_cbranch_scc0 .LBB0_2350
	s_lshl_b32 s12, s12, 7
	v_add_lshl_u32 v132, s24, v160, 1
	s_waitcnt lgkmcnt(0)
	s_barrier
	s_add_i32 s47, s12, 0xffffff00
	v_and_b32_e32 v132, 0xffffff00, v132
	s_and_b32 s13, s33, 0x7f
	v_add_u32_e32 v133, s47, v132
	v_or_b32_e32 v132, s12, v166
	s_lshr_b32 s37, s33, 7
	v_add_u32_e32 v131, s13, v162
	v_cmp_lt_i32_e32 vcc, -1, v133
	v_lshlrev_b32_e32 v132, 7, v132
	v_add_u32_e32 v180, v161, v165
	ds_read_b128 v[176:179], v180
	s_and_saveexec_b64 s[12:13], vcc
	s_cbranch_execz .LBB0_2339
	v_add_u32_e32 v152, v161, v163
	ds_read_b128 v[172:175], v152
	v_lshrrev_b32_e32 v133, 8, v133
	v_mul_u32_u24_e32 v133, s26, v133
	v_add_lshl_u32 v133, v133, s37, 15
	v_and_b32_e32 v152, 0x7f80, v132
	v_add3_u32 v133, v152, v131, v133
	s_waitcnt lgkmcnt(0)
	global_store_dwordx4 v133, v[172:175], s[6:7]

; #define GAS __attribute__((address_space(1)))
; #define LAS __attribute__((address_space(3)))
; #define LDS_BARRIER() do { asm volatile("s_waitcnt lgkmcnt(0)" ::: "memory"); __builtin_amdgcn_s_barrier(); asm volatile("" ::: "memory"); } while (0)
; template <class RowMap>
; __device__ __forceinline__ void conv_store_fp8(const f32x4 (&r)[8], unsigned char* WT, int Kbytes, int k0bytes, int n0, const RowMap rm, LAS unsigned char* T, int tid, int wave, int lane) {
;     ...
;     for (int j = 0; j < 4; ++j) { const unsigned lo = pk4_fp8(r[0][j] * W8_SCALE, r[1][j] * W8_SCALE, r[2][j] * W8_SCALE, r[3][j] * W8_SCALE), hi = pk4_fp8(r[4][j] * W8_SCALE, r[5][j] * W8_SCALE, r[6][j] * W8_SCALE, r[7][j] * W8_SCALE);
;         *(LAS unsigned long long*)(T + (4 * lane + j) * 64 + 8 * (wave ^ s)) = (unsigned long long)lo | ((unsigned long long)hi << 32); }
;     LDS_BARRIER();
;     const int c16 = tid & 3, rr = tid >> 2;
; #pragma unroll
;     for (int q = 0; q < 2; ++q) { const int row = rr + 128 * q; const v4u v = *(const LAS v4u*)(T + row * 64 + 16 * (c16 ^ ((row >> 2) & 3)));
;         const int dr = rm(n0 + row); if (dr >= 0) *(GAS v4u*)(WT + (unsigned)((((dr >> 8) * (Kbytes >> 7) + (k0bytes >> 7)) << 15) + ((dr & 255) << 7) + (k0bytes & 127) + 16 * c16)) = v; }
.Lhw_done_8:
	v_med3_f32 v131, v26, s101, v200
	v_med3_f32 v153, v30, s101, v200
	v_cvt_scalef32_pk_fp8_f32 v132, v131, v153, v201
	v_med3_f32 v133, v34, s101, v200
	v_med3_f32 v152, v38, s101, v200
	v_cvt_scalef32_pk_fp8_f32 v132, v133, v152, v201 op_sel:[0,0,0,1]
	v_med3_f32 v131, v42, s101, v200
	v_med3_f32 v158, v46, s101, v200
	v_cvt_scalef32_pk_fp8_f32 v133, v131, v158, v201
	v_med3_f32 v152, v66, s101, v200
	v_med3_f32 v153, v70, s101, v200
	v_cvt_scalef32_pk_fp8_f32 v133, v152, v153, v201 op_sel:[0,0,0,1]
	v_med3_f32 v131, v27, s101, v200
	v_med3_f32 v159, v31, s101, v200
	v_cvt_scalef32_pk_fp8_f32 v152, v131, v159, v201
	v_med3_f32 v153, v35, s101, v200
	v_med3_f32 v158, v39, s101, v200
	v_cvt_scalef32_pk_fp8_f32 v152, v153, v158, v201 op_sel:[0,0,0,1]
	v_med3_f32 v131, v43, s101, v200
	v_med3_f32 v172, v47, s101, v200
	v_cvt_scalef32_pk_fp8_f32 v153, v131, v172, v201
	v_med3_f32 v158, v67, s101, v200
	v_med3_f32 v159, v71, s101, v200
	v_cvt_scalef32_pk_fp8_f32 v153, v158, v159, v201 op_sel:[0,0,0,1]
	v_med3_f32 v131, v28, s101, v200
	s_cmp_lg_u32 s12, 0
	ds_write2_b64 v171, v[132:133], v[152:153] offset1:8
	v_med3_f32 v153, v32, s101, v200
	v_cvt_scalef32_pk_fp8_f32 v132, v131, v153, v201
	v_med3_f32 v133, v36, s101, v200
	v_med3_f32 v152, v40, s101, v200
	v_cvt_scalef32_pk_fp8_f32 v132, v133, v152, v201 op_sel:[0,0,0,1]
	v_med3_f32 v131, v44, s101, v200
	v_med3_f32 v158, v48, s101, v200
	v_cvt_scalef32_pk_fp8_f32 v133, v131, v158, v201
	v_med3_f32 v152, v68, s101, v200
	v_med3_f32 v153, v72, s101, v200
	v_cvt_scalef32_pk_fp8_f32 v133, v152, v153, v201 op_sel:[0,0,0,1]
	v_med3_f32 v131, v29, s101, v200
	v_med3_f32 v159, v33, s101, v200
	v_cvt_scalef32_pk_fp8_f32 v152, v131, v159, v201
	v_med3_f32 v153, v37, s101, v200
	v_med3_f32 v158, v41, s101, v200
	v_cvt_scalef32_pk_fp8_f32 v152, v153, v158, v201 op_sel:[0,0,0,1]
	v_med3_f32 v131, v45, s101, v200
	v_med3_f32 v172, v49, s101, v200
	v_cvt_scalef32_pk_fp8_f32 v153, v131, v172, v201
	v_med3_f32 v158, v69, s101, v200
	v_med3_f32 v159, v73, s101, v200
	v_cvt_scalef32_pk_fp8_f32 v153, v158, v159, v201 op_sel:[0,0,0,1]
	ds_write2_b64 v171, v[132:133], v[152:153] offset0:16 offset1:24
	s_cbranch_scc0 .LBB0_2375
	s_lshl_b32 s12, s12, 7
	v_add_lshl_u32 v132, s24, v160, 1
	s_waitcnt lgkmcnt(0)
	s_barrier
	s_add_i32 s47, s12, 0xffffff00
	v_and_b32_e32 v132, 0xffffff00, v132
	s_and_b32 s13, s33, 0x7f
	v_add_u32_e32 v133, s47, v132
	v_or_b32_e32 v132, s12, v166
	s_lshr_b32 s37, s33, 7
	v_add_u32_e32 v131, s13, v162
	v_cmp_lt_i32_e32 vcc, -1, v133
	v_lshlrev_b32_e32 v132, 7, v132
	v_add_u32_e32 v180, v161, v165
	ds_read_b128 v[176:179], v180
	s_and_saveexec_b64 s[12:13], vcc
	s_cbranch_execz .LBB0_2372
	v_add_u32_e32 v152, v161, v163
	ds_read_b128 v[172:175], v152
	v_lshrrev_b32_e32 v133, 8, v133
	v_mul_u32_u24_e32 v133, s26, v133
	v_add_lshl_u32 v133, v133, s37, 15
	v_and_b32_e32 v152, 0x7f80, v132
	v_add3_u32 v133, v152, v131, v133
	s_waitcnt lgkmcnt(0)
	global_store_dwordx4 v133, v[172:175], s[6:7]

; #define GAS __attribute__((address_space(1)))
; #define LAS __attribute__((address_space(3)))
; #define LDS_BARRIER() do { asm volatile("s_waitcnt lgkmcnt(0)" ::: "memory"); __builtin_amdgcn_s_barrier(); asm volatile("" ::: "memory"); } while (0)
; template <class RowMap>
; __device__ __forceinline__ void conv_store_fp8(const f32x4 (&r)[8], unsigned char* WT, int Kbytes, int k0bytes, int n0, const RowMap rm, LAS unsigned char* T, int tid, int wave, int lane) {
;     ...
;     for (int j = 0; j < 4; ++j) { const unsigned lo = pk4_fp8(r[0][j] * W8_SCALE, r[1][j] * W8_SCALE, r[2][j] * W8_SCALE, r[3][j] * W8_SCALE), hi = pk4_fp8(r[4][j] * W8_SCALE, r[5][j] * W8_SCALE, r[6][j] * W8_SCALE, r[7][j] * W8_SCALE);
;         *(LAS unsigned long long*)(T + (4 * lane + j) * 64 + 8 * (wave ^ s)) = (unsigned long long)lo | ((unsigned long long)hi << 32); }
;     LDS_BARRIER();
;     const int c16 = tid & 3, rr = tid >> 2;
; #pragma unroll
;     for (int q = 0; q < 2; ++q) { const int row = rr + 128 * q; const v4u v = *(const LAS v4u*)(T + row * 64 + 16 * (c16 ^ ((row >> 2) & 3)));
;         const int dr = rm(n0 + row); if (dr >= 0) *(GAS v4u*)(WT + (unsigned)((((dr >> 8) * (Kbytes >> 7) + (k0bytes >> 7)) << 15) + ((dr & 255) << 7) + (k0bytes & 127) + 16 * c16)) = v; }
.Lhw_done_9:
	v_med3_f32 v131, v58, s101, v200
	v_med3_f32 v153, v62, s101, v200
	v_cvt_scalef32_pk_fp8_f32 v132, v131, v153, v201
	v_med3_f32 v133, v74, s101, v200
	v_med3_f32 v152, v78, s101, v200
	v_cvt_scalef32_pk_fp8_f32 v132, v133, v152, v201 op_sel:[0,0,0,1]
	v_med3_f32 v131, v82, s101, v200
	v_med3_f32 v158, v86, s101, v200
	v_cvt_scalef32_pk_fp8_f32 v133, v131, v158, v201
	v_med3_f32 v152, v102, s101, v200
	v_med3_f32 v153, v106, s101, v200
	v_cvt_scalef32_pk_fp8_f32 v133, v152, v153, v201 op_sel:[0,0,0,1]
	v_med3_f32 v131, v59, s101, v200
	v_med3_f32 v159, v63, s101, v200
	v_cvt_scalef32_pk_fp8_f32 v152, v131, v159, v201
	v_med3_f32 v153, v75, s101, v200
	v_med3_f32 v158, v79, s101, v200
	v_cvt_scalef32_pk_fp8_f32 v152, v153, v158, v201 op_sel:[0,0,0,1]
	v_med3_f32 v131, v83, s101, v200
	v_med3_f32 v172, v87, s101, v200
	v_cvt_scalef32_pk_fp8_f32 v153, v131, v172, v201
	v_med3_f32 v158, v103, s101, v200
	v_med3_f32 v159, v107, s101, v200
	v_cvt_scalef32_pk_fp8_f32 v153, v158, v159, v201 op_sel:[0,0,0,1]
	v_med3_f32 v131, v60, s101, v200
	s_cmp_lg_u32 s12, 0
	ds_write2_b64 v171, v[132:133], v[152:153] offset1:8
	v_med3_f32 v153, v64, s101, v200
	v_cvt_scalef32_pk_fp8_f32 v132, v131, v153, v201
	v_med3_f32 v133, v76, s101, v200
	v_med3_f32 v152, v80, s101, v200
	v_cvt_scalef32_pk_fp8_f32 v132, v133, v152, v201 op_sel:[0,0,0,1]
	v_med3_f32 v131, v84, s101, v200
	v_med3_f32 v158, v88, s101, v200
	v_cvt_scalef32_pk_fp8_f32 v133, v131, v158, v201
	v_med3_f32 v152, v104, s101, v200
	v_med3_f32 v153, v108, s101, v200
	v_cvt_scalef32_pk_fp8_f32 v133, v152, v153, v201 op_sel:[0,0,0,1]
	v_med3_f32 v131, v61, s101, v200
	v_med3_f32 v159, v65, s101, v200
	v_cvt_scalef32_pk_fp8_f32 v152, v131, v159, v201
	v_med3_f32 v153, v77, s101, v200
	v_med3_f32 v158, v81, s101, v200
	v_cvt_scalef32_pk_fp8_f32 v152, v153, v158, v201 op_sel:[0,0,0,1]
	v_med3_f32 v131, v85, s101, v200
	v_med3_f32 v172, v89, s101, v200
	v_cvt_scalef32_pk_fp8_f32 v153, v131, v172, v201
	v_med3_f32 v158, v105, s101, v200
	v_med3_f32 v159, v109, s101, v200
	v_cvt_scalef32_pk_fp8_f32 v153, v158, v159, v201 op_sel:[0,0,0,1]
	ds_write2_b64 v171, v[132:133], v[152:153] offset0:16 offset1:24
	s_cbranch_scc0 .LBB0_2407
	s_lshl_b32 s12, s12, 7
	v_add_lshl_u32 v132, s24, v160, 1
	s_waitcnt lgkmcnt(0)
	s_barrier
	s_add_i32 s47, s12, 0xffffff00
	v_and_b32_e32 v132, 0xffffff00, v132
	s_and_b32 s13, s33, 0x7f
	v_add_u32_e32 v133, s47, v132
	v_or_b32_e32 v132, s12, v166
	s_lshr_b32 s37, s33, 7
	v_add_u32_e32 v131, s13, v162
	v_cmp_lt_i32_e32 vcc, -1, v133
	v_lshlrev_b32_e32 v132, 7, v132
	v_add_u32_e32 v180, v161, v165
	ds_read_b128 v[176:179], v180
	s_and_saveexec_b64 s[12:13], vcc
	s_cbranch_execz .LBB0_2404
	v_add_u32_e32 v152, v161, v163
	ds_read_b128 v[172:175], v152
	v_lshrrev_b32_e32 v133, 8, v133
	v_mul_u32_u24_e32 v133, s26, v133
	v_add_lshl_u32 v133, v133, s37, 15
	v_and_b32_e32 v152, 0x7f80, v132
	v_add3_u32 v133, v152, v131, v133
	s_waitcnt lgkmcnt(0)
	global_store_dwordx4 v133, v[172:175], s[6:7]

; #define GAS __attribute__((address_space(1)))
; #define LAS __attribute__((address_space(3)))
; #define LDS_BARRIER() do { asm volatile("s_waitcnt lgkmcnt(0)" ::: "memory"); __builtin_amdgcn_s_barrier(); asm volatile("" ::: "memory"); } while (0)
; template <class RowMap>
; __device__ __forceinline__ void conv_store_fp8(const f32x4 (&r)[8], unsigned char* WT, int Kbytes, int k0bytes, int n0, const RowMap rm, LAS unsigned char* T, int tid, int wave, int lane) {
;     ...
;     for (int j = 0; j < 4; ++j) { const unsigned lo = pk4_fp8(r[0][j] * W8_SCALE, r[1][j] * W8_SCALE, r[2][j] * W8_SCALE, r[3][j] * W8_SCALE), hi = pk4_fp8(r[4][j] * W8_SCALE, r[5][j] * W8_SCALE, r[6][j] * W8_SCALE, r[7][j] * W8_SCALE);
;         *(LAS unsigned long long*)(T + (4 * lane + j) * 64 + 8 * (wave ^ s)) = (unsigned long long)lo | ((unsigned long long)hi << 32); }
;     LDS_BARRIER();
;     const int c16 = tid & 3, rr = tid >> 2;
; #pragma unroll
;     for (int q = 0; q < 2; ++q) { const int row = rr + 128 * q; const v4u v = *(const LAS v4u*)(T + row * 64 + 16 * (c16 ^ ((row >> 2) & 3)));
;         const int dr = rm(n0 + row); if (dr >= 0) *(GAS v4u*)(WT + (unsigned)((((dr >> 8) * (Kbytes >> 7) + (k0bytes >> 7)) << 15) + ((dr & 255) << 7) + (k0bytes & 127) + 16 * c16)) = v; }
.Lhw_done_10:
	v_med3_f32 v131, v94, s101, v200
	v_med3_f32 v153, v98, s101, v200
	v_cvt_scalef32_pk_fp8_f32 v132, v131, v153, v201
	v_med3_f32 v133, v90, s101, v200
	v_med3_f32 v152, v110, s101, v200
	v_cvt_scalef32_pk_fp8_f32 v132, v133, v152, v201 op_sel:[0,0,0,1]
	v_med3_f32 v131, v114, s101, v200
	v_med3_f32 v158, v118, s101, v200
	v_cvt_scalef32_pk_fp8_f32 v133, v131, v158, v201
	v_med3_f32 v152, v126, s101, v200
	v_med3_f32 v153, v122, s101, v200
	v_cvt_scalef32_pk_fp8_f32 v133, v152, v153, v201 op_sel:[0,0,0,1]
	v_med3_f32 v131, v95, s101, v200
	v_med3_f32 v159, v99, s101, v200
	v_cvt_scalef32_pk_fp8_f32 v152, v131, v159, v201
	v_med3_f32 v153, v91, s101, v200
	v_med3_f32 v158, v111, s101, v200
	v_cvt_scalef32_pk_fp8_f32 v152, v153, v158, v201 op_sel:[0,0,0,1]
	v_med3_f32 v131, v115, s101, v200
	v_med3_f32 v172, v119, s101, v200
	v_cvt_scalef32_pk_fp8_f32 v153, v131, v172, v201
	v_med3_f32 v158, v127, s101, v200
	v_med3_f32 v159, v123, s101, v200
	v_cvt_scalef32_pk_fp8_f32 v153, v158, v159, v201 op_sel:[0,0,0,1]
	v_med3_f32 v131, v96, s101, v200
	s_cmp_lg_u32 s6, 0
	ds_write2_b64 v171, v[132:133], v[152:153] offset1:8
	v_med3_f32 v153, v100, s101, v200
	v_cvt_scalef32_pk_fp8_f32 v132, v131, v153, v201
	v_med3_f32 v133, v92, s101, v200
	v_med3_f32 v152, v112, s101, v200
	v_cvt_scalef32_pk_fp8_f32 v132, v133, v152, v201 op_sel:[0,0,0,1]
	v_med3_f32 v131, v116, s101, v200
	v_med3_f32 v158, v120, s101, v200
	v_cvt_scalef32_pk_fp8_f32 v133, v131, v158, v201
	v_med3_f32 v152, v128, s101, v200
	v_med3_f32 v153, v124, s101, v200
	v_cvt_scalef32_pk_fp8_f32 v133, v152, v153, v201 op_sel:[0,0,0,1]
	v_med3_f32 v131, v97, s101, v200
	v_med3_f32 v159, v101, s101, v200
	v_cvt_scalef32_pk_fp8_f32 v152, v131, v159, v201
	v_med3_f32 v153, v93, s101, v200
	v_med3_f32 v158, v113, s101, v200
	v_cvt_scalef32_pk_fp8_f32 v152, v153, v158, v201 op_sel:[0,0,0,1]
	v_med3_f32 v131, v117, s101, v200
	v_med3_f32 v172, v121, s101, v200
	v_cvt_scalef32_pk_fp8_f32 v153, v131, v172, v201
	v_med3_f32 v158, v129, s101, v200
	v_med3_f32 v159, v125, s101, v200
	v_cvt_scalef32_pk_fp8_f32 v153, v158, v159, v201 op_sel:[0,0,0,1]
	ds_write2_b64 v171, v[132:133], v[152:153] offset0:16 offset1:24
	s_cbranch_scc0 .LBB0_2439
	s_lshl_b32 s6, s6, 7
	v_add_lshl_u32 v132, s2, v160, 1
	s_waitcnt lgkmcnt(0)
	s_barrier
	s_add_i32 s24, s6, 0xffffff00
	v_and_b32_e32 v132, 0xffffff00, v132
	s_and_b32 s7, s13, 0x7f
	v_add_u32_e32 v133, s24, v132
	v_or_b32_e32 v132, s6, v166
	s_lshr_b32 s18, s13, 7
	v_add_u32_e32 v131, s7, v162
	v_cmp_lt_i32_e32 vcc, -1, v133
	v_lshlrev_b32_e32 v132, 7, v132
	v_add_u32_e32 v180, v161, v165
	ds_read_b128 v[176:179], v180
	s_and_saveexec_b64 s[6:7], vcc
	s_cbranch_execz .LBB0_2436
	v_add_u32_e32 v152, v161, v163
	ds_read_b128 v[172:175], v152
	v_lshrrev_b32_e32 v133, 8, v133
	v_mul_u32_u24_e32 v133, s12, v133
	v_add_lshl_u32 v133, v133, s18, 15
	v_and_b32_e32 v152, 0x7f80, v132
	v_add3_u32 v133, v152, v131, v133
	s_waitcnt lgkmcnt(0)
	global_store_dwordx4 v133, v[172:175], s[4:5]
